# E9: E8 + in-place fmax canonicalisations (identity for non-sNaN) removed from the G1/G2 epilogues
# baseline (speedup 1.0000x reference)
.LBB0_1219:
	s_ashr_i32 s45, s44, 31
	s_lshl_b64 s[42:43], s[44:45], 9
	s_add_u32 s42, s55, s42
	v_mov_b32_e32 v0, v1
	s_addc_u32 s43, s56, s43
	global_load_dwordx2 v[172:173], v0, s[42:43]
	v_readlane_b32 s72, v252, 13
	s_ashr_i32 s41, s40, 31
	v_readlane_b32 s74, v252, 15
	v_readlane_b32 s75, v252, 16
	v_readlane_b32 s78, v252, 19
	v_readlane_b32 s79, v252, 20
	s_lshl_b64 s[40:41], s[40:41], 14
	s_mov_b64 s[74:75], s[78:79]
	v_lshl_or_b32 v176, s10, 7, v174
	s_add_u32 s42, s74, s40
	s_addc_u32 s43, s75, s41
	v_ashrrev_i32_e32 v177, 31, v176
	v_lshl_add_u64 v[78:79], v[176:177], 2, s[42:43]
	v_readlane_b32 s42, v252, 48
	v_readlane_b32 s43, v252, 49
	s_add_u32 s35, s42, s40
	s_addc_u32 s37, s43, s41
	s_lshl_b32 s40, s10, 8
	s_ashr_i32 s41, s40, 31
	s_lshl_b64 s[40:41], s[40:41], 2
	v_lshl_add_u32 v178, s16, 8, v188
	s_add_u32 s40, s35, s40
	v_ashrrev_i32_e32 v179, 31, v178
	s_addc_u32 s41, s37, s41
	v_lshlrev_b32_e32 v80, 2, v174
	v_lshl_add_u64 v[180:181], v[178:179], 2, s[20:21]
	global_load_dwordx4 v[70:73], v80, s[40:41] offset:16
	global_load_dwordx4 v[98:101], v80, s[40:41]
	global_load_dword v0, v[180:181], off
	global_load_dwordx4 v[74:77], v80, s[40:41] offset:528
	global_load_dwordx4 v[102:105], v80, s[40:41] offset:512
	global_load_dwordx4 v[106:109], v[78:79], off
	v_add_co_u32_e32 v80, vcc, s61, v78
	v_cvt_f32_i32_e32 v182, v158
	s_nop 0
	v_addc_co_u32_e32 v81, vcc, 0, v79, vcc
	global_load_dwordx4 v[94:97], v[80:81], off
	global_load_dwordx4 v[82:85], v[78:79], off offset:16
	v_lshl_add_u64 v[78:79], v[78:79], 0, s[28:29]
	global_load_dwordx4 v[78:81], v[78:79], off offset:16
	v_cvt_f32_i32_e32 v184, v154
	v_cvt_f32_i32_e32 v194, v160
	v_cvt_f32_i32_e32 v196, v156
	v_cvt_f32_i32_e32 v198, v150
	v_cvt_f32_i32_e32 v200, v146
	v_cvt_f32_i32_e32 v202, v152
	global_load_dword v160, v[180:181], off offset:64
	global_load_dword v158, v[180:181], off offset:128
	global_load_dword v156, v[180:181], off offset:192
	global_load_dword v154, v[180:181], off offset:512
	global_load_dword v152, v[180:181], off offset:576
	global_load_dword v150, v[180:181], off offset:640
	global_load_dword v146, v[180:181], off offset:704
	v_cvt_f32_i32_e32 v183, v159
	v_cvt_f32_i32_e32 v185, v155
	v_cvt_f32_i32_e32 v195, v161
	v_cvt_f32_i32_e32 v197, v157
	v_cvt_f32_i32_e32 v199, v151
	v_cvt_f32_i32_e32 v201, v147
	v_cvt_f32_i32_e32 v203, v153
	v_cvt_f32_i32_e32 v149, v149
	v_cvt_f32_i32_e32 v148, v148
	v_readlane_b32 s73, v252, 14
	v_readlane_b32 s76, v252, 17
	v_readlane_b32 s77, v252, 18
	v_readlane_b32 s80, v252, 21
	v_readlane_b32 s81, v252, 22
	v_readlane_b32 s82, v252, 23
	v_readlane_b32 s83, v252, 24
	v_readlane_b32 s84, v252, 25
	v_readlane_b32 s85, v252, 26
	v_readlane_b32 s86, v252, 27
	v_readlane_b32 s87, v252, 28
	s_waitcnt vmcnt(0)
	v_pk_mul_f32 v[212:213], v[74:75], v[0:1] op_sel_hi:[1,0]
	v_pk_mul_f32 v[180:181], v[98:99], v[0:1] op_sel_hi:[1,0]
	v_pk_mul_f32 v[204:205], v[102:103], v[0:1] op_sel_hi:[1,0]
	v_pk_mul_f32 v[206:207], v[100:101], v[0:1] op_sel_hi:[1,0]
	v_pk_fma_f32 v[180:181], v[182:183], v[180:181], v[106:107]
	v_pk_mul_f32 v[208:209], v[104:105], v[0:1] op_sel_hi:[1,0]
	v_pk_mul_f32 v[210:211], v[70:71], v[0:1] op_sel_hi:[1,0]
	v_pk_fma_f32 v[182:183], v[184:185], v[204:205], v[94:95]
	v_pk_fma_f32 v[184:185], v[194:195], v[206:207], v[108:109]
	v_min_f32_e32 v180, 0x40e00000, v180
	v_min_f32_e32 v181, 0x40e00000, v181
	v_min_f32_e32 v184, 0x40e00000, v184
	v_min_f32_e32 v185, 0x40e00000, v185
	v_pk_fma_f32 v[194:195], v[196:197], v[208:209], v[96:97]
	v_pk_fma_f32 v[196:197], v[198:199], v[210:211], v[82:83]
	v_pk_fma_f32 v[198:199], v[200:201], v[212:213], v[78:79]
	v_pk_mul_f32 v[200:201], v[180:181], s[30:31] op_sel_hi:[1,0]
	v_pk_mul_f32 v[204:205], v[184:185], s[30:31] op_sel_hi:[1,0]
	v_exp_f32_e32 v200, v200
	v_exp_f32_e32 v201, v201
	v_exp_f32_e32 v204, v204
	v_exp_f32_e32 v205, v205
	v_min_f32_e32 v196, 0x40e00000, v196
	v_min_f32_e32 v197, 0x40e00000, v197
	v_pk_mul_f32 v[206:207], v[196:197], s[30:31] op_sel_hi:[1,0]
	v_pk_add_f32 v[200:201], v[200:201], 1.0 op_sel_hi:[1,0]
	v_exp_f32_e32 v206, v206
	v_exp_f32_e32 v207, v207
	v_pk_add_f32 v[204:205], v[204:205], 1.0 op_sel_hi:[1,0]
	v_rcp_f32_e32 v200, v200
	v_rcp_f32_e32 v201, v201
	v_rcp_f32_e32 v204, v204
	v_rcp_f32_e32 v205, v205
	v_pk_add_f32 v[206:207], v[206:207], 1.0 op_sel_hi:[1,0]
	v_med3_f32 v182, v182, s69, v193
	v_med3_f32 v183, v183, s69, v193
	v_med3_f32 v194, v194, s69, v193
	v_med3_f32 v195, v195, s69, v193
	v_rcp_f32_e32 v206, v206
	v_rcp_f32_e32 v207, v207
	v_pk_add_f32 v[182:183], v[182:183], 1.0 op_sel_hi:[1,0]
	v_pk_add_f32 v[194:195], v[194:195], 1.0 op_sel_hi:[1,0]
	v_pk_mul_f32 v[180:181], v[180:181], v[200:201]
	v_pk_mul_f32 v[184:185], v[184:185], v[204:205]
	v_pk_mul_f32 v[180:181], v[182:183], v[180:181]
	v_pk_mul_f32 v[182:183], v[194:195], v[184:185]
	v_pk_mul_f32 v[194:195], v[72:73], v[0:1] op_sel_hi:[1,0]
	v_med3_f32 v198, v198, s69, v193
	v_med3_f32 v199, v199, s69, v193
	v_pk_fma_f32 v[194:195], v[202:203], v[194:195], v[84:85]
	v_pk_add_f32 v[198:199], v[198:199], 1.0 op_sel_hi:[1,0]
	v_pk_mul_f32 v[196:197], v[196:197], v[206:207]
	v_min_f32_e32 v194, 0x40e00000, v194
	v_min_f32_e32 v195, 0x40e00000, v195
	v_pk_mul_f32 v[184:185], v[198:199], v[196:197]
	v_pk_mul_f32 v[196:197], v[194:195], s[30:31] op_sel_hi:[1,0]
	v_pk_mul_f32 v[198:199], v[76:77], v[0:1] op_sel_hi:[1,0]
	v_exp_f32_e32 v196, v196
	v_exp_f32_e32 v197, v197
	v_pk_fma_f32 v[148:149], v[148:149], v[198:199], v[80:81]
	v_max_f32_e64 v147, |v180|, |v181|
	v_med3_f32 v148, v148, s69, v193
	v_pk_add_f32 v[196:197], v[196:197], 1.0 op_sel_hi:[1,0]
	v_med3_f32 v149, v149, s69, v193
	v_rcp_f32_e32 v196, v196
	v_rcp_f32_e32 v197, v197
	v_pk_add_f32 v[148:149], v[148:149], 1.0 op_sel_hi:[1,0]
	v_max_f32_e64 v151, |v182|, |v183|
	v_max3_f32 v147, v147, 0, v151
	v_pk_mul_f32 v[194:195], v[194:195], v[196:197]
	v_max_f32_e64 v151, |v184|, |v185|
	v_pk_mul_f32 v[148:149], v[148:149], v[194:195]
	s_nop 0
	v_max_f32_e64 v0, |v148|, |v149|
	v_max3_f32 v0, v147, v151, v0
	v_mov_b32_e32 v147, v0
	s_nop 1
	v_permlane16_swap_b32_e32 v0, v147
	v_max_f32_e32 v0, v0, v147
	v_mov_b32_e32 v147, v0
	s_nop 1
	v_permlane32_swap_b32_e32 v0, v147
	v_max_f32_e32 v147, v0, v147
	s_and_saveexec_b64 s[40:41], s[4:5]
	s_cbranch_execz .LBB0_1221
	v_lshlrev_b64 v[194:195], 8, v[178:179]
	s_lshl_b32 s42, s10, 2
	v_lshl_add_u64 v[194:195], s[12:13], 0, v[194:195]
	s_ashr_i32 s43, s42, 31
	v_lshl_add_u64 v[194:195], s[42:43], 2, v[194:195]
	s_lshl_b32 s16, s62, 2
	v_lshl_add_u64 v[194:195], v[194:195], 0, s[16:17]
	global_store_dword v[194:195], v147, off
.LBB0_1221:
	s_or_b64 exec, exec, s[40:41]
	v_rcp_f32_e32 v0, v147
	v_cmp_lt_f32_e32 vcc, 0, v147
	v_cvt_f32_i32_e32 v143, v143
	v_cvt_f32_i32_e32 v142, v142
	v_mul_f32_e32 v0, 0x42fe0000, v0
	v_cndmask_b32_e32 v0, 0, v0, vcc
	v_pk_mul_f32 v[180:181], v[0:1], v[180:181] op_sel_hi:[0,1]
	v_pk_mul_f32 v[182:183], v[0:1], v[182:183] op_sel_hi:[0,1]
	v_pk_mul_f32 v[184:185], v[0:1], v[184:185] op_sel_hi:[0,1]
	v_pk_mul_f32 v[148:149], v[0:1], v[148:149] op_sel_hi:[0,1]
	v_add_f32_e32 v0, 0x4b400000, v180
	v_add_f32_e32 v147, 0x4b400000, v181
	v_add_f32_e32 v151, 0x4b400000, v182
	v_add_f32_e32 v153, 0x4b400000, v183
	v_perm_b32 v0, v147, v0, s70
	v_perm_b32 v147, v153, v151, s70
	v_lshl_or_b32 v180, v147, 16, v0
	v_add_f32_e32 v0, 0x4b400000, v184
	v_add_f32_e32 v147, 0x4b400000, v185
	v_add_f32_e32 v148, 0x4b400000, v148
	v_add_f32_e32 v149, 0x4b400000, v149
	v_perm_b32 v0, v147, v0, s70
	v_perm_b32 v147, v149, v148, s70
	v_lshlrev_b64 v[148:149], 11, v[178:179]
	v_lshl_add_u64 v[148:149], s[2:3], 0, v[148:149]
	v_lshl_or_b32 v181, v147, 16, v0
	v_lshl_add_u64 v[148:149], v[148:149], 0, v[176:177]
	global_store_dwordx2 v[148:149], v[180:181], off
	v_pk_mul_f32 v[148:149], v[98:99], v[160:161] op_sel_hi:[1,0]
	v_cvt_f32_i32_e32 v139, v139
	v_pk_fma_f32 v[142:143], v[142:143], v[148:149], v[106:107]
	v_cvt_f32_i32_e32 v138, v138
	v_min_f32_e32 v142, 0x40e00000, v142
	v_min_f32_e32 v143, 0x40e00000, v143
	v_pk_mul_f32 v[148:149], v[142:143], s[30:31] op_sel_hi:[1,0]
	v_pk_mul_f32 v[180:181], v[102:103], v[160:161] op_sel_hi:[1,0]
	v_exp_f32_e32 v148, v148
	v_exp_f32_e32 v149, v149
	v_pk_fma_f32 v[138:139], v[138:139], v[180:181], v[94:95]
	v_cvt_f32_i32_e32 v145, v145
	v_cvt_f32_i32_e32 v144, v144
	v_pk_add_f32 v[148:149], v[148:149], 1.0 op_sel_hi:[1,0]
	v_med3_f32 v138, v138, s69, v193
	v_rcp_f32_e32 v148, v148
	v_rcp_f32_e32 v149, v149
	v_med3_f32 v139, v139, s69, v193
	v_pk_add_f32 v[138:139], v[138:139], 1.0 op_sel_hi:[1,0]
	v_cvt_f32_i32_e32 v141, v141
	v_pk_mul_f32 v[142:143], v[142:143], v[148:149]
	v_cvt_f32_i32_e32 v140, v140
	v_pk_mul_f32 v[138:139], v[138:139], v[142:143]
	v_pk_mul_f32 v[142:143], v[100:101], v[160:161] op_sel_hi:[1,0]
	v_pk_mul_f32 v[148:149], v[104:105], v[160:161] op_sel_hi:[1,0]
	v_pk_fma_f32 v[142:143], v[144:145], v[142:143], v[108:109]
	v_pk_fma_f32 v[140:141], v[140:141], v[148:149], v[96:97]
	v_min_f32_e32 v142, 0x40e00000, v142
	v_min_f32_e32 v143, 0x40e00000, v143
	v_pk_mul_f32 v[144:145], v[142:143], s[30:31] op_sel_hi:[1,0]
	v_med3_f32 v140, v140, s69, v193
	v_exp_f32_e32 v144, v144
	v_exp_f32_e32 v145, v145
	v_med3_f32 v141, v141, s69, v193
	v_pk_add_f32 v[140:141], v[140:141], 1.0 op_sel_hi:[1,0]
	v_cvt_f32_i32_e32 v135, v135
	v_pk_add_f32 v[144:145], v[144:145], 1.0 op_sel_hi:[1,0]
	v_cvt_f32_i32_e32 v134, v134
	v_rcp_f32_e32 v144, v144
	v_rcp_f32_e32 v145, v145
	v_max_f32_e64 v0, |v138|, |v139|
	v_cvt_f32_i32_e32 v131, v131
	v_cvt_f32_i32_e32 v130, v130
	v_pk_mul_f32 v[142:143], v[142:143], v[144:145]
	v_pk_mul_f32 v[144:145], v[74:75], v[160:161] op_sel_hi:[1,0]
	v_pk_mul_f32 v[140:141], v[140:141], v[142:143]
	v_pk_fma_f32 v[130:131], v[130:131], v[144:145], v[78:79]
	v_max_f32_e64 v142, |v140|, |v141|
	v_max3_f32 v0, v0, 0, v142
	v_pk_mul_f32 v[142:143], v[70:71], v[160:161] op_sel_hi:[1,0]
	v_cvt_f32_i32_e32 v137, v137
	v_pk_fma_f32 v[134:135], v[134:135], v[142:143], v[82:83]
	v_cvt_f32_i32_e32 v136, v136
	v_min_f32_e32 v134, 0x40e00000, v134
	v_min_f32_e32 v135, 0x40e00000, v135
	v_pk_mul_f32 v[142:143], v[134:135], s[30:31] op_sel_hi:[1,0]
	v_med3_f32 v130, v130, s69, v193
	v_exp_f32_e32 v142, v142
	v_exp_f32_e32 v143, v143
	v_med3_f32 v131, v131, s69, v193
	v_pk_add_f32 v[130:131], v[130:131], 1.0 op_sel_hi:[1,0]
	v_cvt_f32_i32_e32 v133, v133
	v_pk_add_f32 v[142:143], v[142:143], 1.0 op_sel_hi:[1,0]
	v_cvt_f32_i32_e32 v132, v132
	v_rcp_f32_e32 v142, v142
	v_rcp_f32_e32 v143, v143
	s_nop 0
	v_pk_mul_f32 v[134:135], v[134:135], v[142:143]
	s_nop 0
	v_pk_mul_f32 v[130:131], v[130:131], v[134:135]
	v_pk_mul_f32 v[134:135], v[72:73], v[160:161] op_sel_hi:[1,0]
	v_pk_mul_f32 v[142:143], v[76:77], v[160:161] op_sel_hi:[1,0]
	v_pk_fma_f32 v[134:135], v[136:137], v[134:135], v[84:85]
	v_pk_fma_f32 v[132:133], v[132:133], v[142:143], v[80:81]
	v_min_f32_e32 v134, 0x40e00000, v134
	v_min_f32_e32 v135, 0x40e00000, v135
	v_pk_mul_f32 v[136:137], v[134:135], s[30:31] op_sel_hi:[1,0]
	v_med3_f32 v132, v132, s69, v193
	v_exp_f32_e32 v136, v136
	v_exp_f32_e32 v137, v137
	v_med3_f32 v133, v133, s69, v193
	v_pk_add_f32 v[132:133], v[132:133], 1.0 op_sel_hi:[1,0]
	v_max_f32_e64 v144, |v130|, |v131|
	v_pk_add_f32 v[136:137], v[136:137], 1.0 op_sel_hi:[1,0]
	s_nop 0
	v_rcp_f32_e32 v136, v136
	v_rcp_f32_e32 v137, v137
	s_nop 0
	v_pk_mul_f32 v[134:135], v[134:135], v[136:137]
	s_nop 0
	v_pk_mul_f32 v[134:135], v[132:133], v[134:135]
	s_nop 0
	v_max_f32_e64 v132, |v134|, |v135|
	v_max3_f32 v0, v0, v144, v132
	v_mov_b32_e32 v133, v0
	s_nop 1
	v_permlane16_swap_b32_e32 v0, v133
	v_max_f32_e32 v0, v0, v133
	v_mov_b32_e32 v133, v0
	s_nop 1
	v_permlane32_swap_b32_e32 v0, v133
	v_or_b32_e32 v132, 16, v178
	v_max_f32_e32 v136, v0, v133
	v_ashrrev_i32_e32 v133, 31, v132
	s_and_saveexec_b64 s[40:41], s[4:5]
	s_cbranch_execz .LBB0_1223
	s_lshl_b32 s42, s10, 2
	v_lshlrev_b64 v[142:143], 8, v[132:133]
	s_ashr_i32 s43, s42, 31
	v_lshl_add_u64 v[142:143], s[12:13], 0, v[142:143]
	v_lshl_add_u64 v[142:143], s[42:43], 2, v[142:143]
	s_lshl_b32 s16, s62, 2
	v_lshl_add_u64 v[142:143], v[142:143], 0, s[16:17]
	global_store_dword v[142:143], v136, off
.LBB0_1223:
	s_or_b64 exec, exec, s[40:41]
	v_rcp_f32_e32 v0, v136
	v_cmp_lt_f32_e32 vcc, 0, v136
	v_cvt_f32_i32_e32 v127, v127
	v_cvt_f32_i32_e32 v126, v126
	v_mul_f32_e32 v0, 0x42fe0000, v0
	v_cndmask_b32_e32 v0, 0, v0, vcc
	v_pk_mul_f32 v[136:137], v[138:139], v[0:1] op_sel_hi:[1,0]
	v_pk_mul_f32 v[138:139], v[140:141], v[0:1] op_sel_hi:[1,0]
	v_pk_mul_f32 v[130:131], v[130:131], v[0:1] op_sel_hi:[1,0]
	v_pk_mul_f32 v[134:135], v[134:135], v[0:1] op_sel_hi:[1,0]
	v_add_f32_e32 v0, 0x4b400000, v136
	v_add_f32_e32 v136, 0x4b400000, v137
	v_add_f32_e32 v137, 0x4b400000, v138
	v_add_f32_e32 v138, 0x4b400000, v139
	v_perm_b32 v0, v136, v0, s70
	v_perm_b32 v136, v138, v137, s70
	v_lshl_or_b32 v136, v136, 16, v0
	v_add_f32_e32 v0, 0x4b400000, v130
	v_add_f32_e32 v130, 0x4b400000, v131
	v_add_f32_e32 v131, 0x4b400000, v134
	v_add_f32_e32 v134, 0x4b400000, v135
	v_perm_b32 v0, v130, v0, s70
	v_perm_b32 v130, v134, v131, s70
	v_lshl_or_b32 v137, v130, 16, v0
	v_lshlrev_b64 v[130:131], 11, v[132:133]
	v_lshl_add_u64 v[130:131], s[2:3], 0, v[130:131]
	v_lshl_add_u64 v[130:131], v[130:131], 0, v[176:177]
	global_store_dwordx2 v[130:131], v[136:137], off
	v_pk_mul_f32 v[130:131], v[98:99], v[158:159] op_sel_hi:[1,0]
	v_cvt_f32_i32_e32 v123, v123
	v_pk_fma_f32 v[126:127], v[126:127], v[130:131], v[106:107]
	v_cvt_f32_i32_e32 v122, v122
	v_min_f32_e32 v126, 0x40e00000, v126
	v_min_f32_e32 v127, 0x40e00000, v127
	v_pk_mul_f32 v[130:131], v[126:127], s[30:31] op_sel_hi:[1,0]
	v_pk_mul_f32 v[132:133], v[102:103], v[158:159] op_sel_hi:[1,0]
	v_exp_f32_e32 v130, v130
	v_exp_f32_e32 v131, v131
	v_pk_fma_f32 v[122:123], v[122:123], v[132:133], v[94:95]
	v_cvt_f32_i32_e32 v129, v129
	v_cvt_f32_i32_e32 v128, v128
	v_pk_add_f32 v[130:131], v[130:131], 1.0 op_sel_hi:[1,0]
	v_med3_f32 v122, v122, s69, v193
	v_rcp_f32_e32 v130, v130
	v_rcp_f32_e32 v131, v131
	v_med3_f32 v123, v123, s69, v193
	v_pk_add_f32 v[122:123], v[122:123], 1.0 op_sel_hi:[1,0]
	v_cvt_f32_i32_e32 v125, v125
	v_pk_mul_f32 v[126:127], v[126:127], v[130:131]
	v_cvt_f32_i32_e32 v124, v124
	v_pk_mul_f32 v[122:123], v[122:123], v[126:127]
	v_pk_mul_f32 v[126:127], v[100:101], v[158:159] op_sel_hi:[1,0]
	v_pk_mul_f32 v[130:131], v[104:105], v[158:159] op_sel_hi:[1,0]
	v_pk_fma_f32 v[126:127], v[128:129], v[126:127], v[108:109]
	v_pk_fma_f32 v[124:125], v[124:125], v[130:131], v[96:97]
	v_min_f32_e32 v126, 0x40e00000, v126
	v_min_f32_e32 v127, 0x40e00000, v127
	v_pk_mul_f32 v[128:129], v[126:127], s[30:31] op_sel_hi:[1,0]
	v_med3_f32 v124, v124, s69, v193
	v_exp_f32_e32 v128, v128
	v_exp_f32_e32 v129, v129
	v_med3_f32 v125, v125, s69, v193
	v_pk_add_f32 v[124:125], v[124:125], 1.0 op_sel_hi:[1,0]
	v_cvt_f32_i32_e32 v119, v119
	v_pk_add_f32 v[128:129], v[128:129], 1.0 op_sel_hi:[1,0]
	v_cvt_f32_i32_e32 v118, v118
	v_rcp_f32_e32 v128, v128
	v_rcp_f32_e32 v129, v129
	v_max_f32_e64 v0, |v122|, |v123|
	v_cvt_f32_i32_e32 v115, v115
	v_cvt_f32_i32_e32 v114, v114
	v_pk_mul_f32 v[126:127], v[126:127], v[128:129]
	v_pk_mul_f32 v[128:129], v[74:75], v[158:159] op_sel_hi:[1,0]
	v_pk_mul_f32 v[124:125], v[124:125], v[126:127]
	v_pk_fma_f32 v[114:115], v[114:115], v[128:129], v[78:79]
	v_max_f32_e64 v126, |v124|, |v125|
	v_max3_f32 v0, v0, 0, v126
	v_pk_mul_f32 v[126:127], v[70:71], v[158:159] op_sel_hi:[1,0]
	v_cvt_f32_i32_e32 v121, v121
	v_pk_fma_f32 v[118:119], v[118:119], v[126:127], v[82:83]
	v_cvt_f32_i32_e32 v120, v120
	v_min_f32_e32 v118, 0x40e00000, v118
	v_min_f32_e32 v119, 0x40e00000, v119
	v_pk_mul_f32 v[126:127], v[118:119], s[30:31] op_sel_hi:[1,0]
	v_med3_f32 v114, v114, s69, v193
	v_exp_f32_e32 v126, v126
	v_exp_f32_e32 v127, v127
	v_med3_f32 v115, v115, s69, v193
	v_pk_add_f32 v[114:115], v[114:115], 1.0 op_sel_hi:[1,0]
	v_cvt_f32_i32_e32 v117, v117
	v_pk_add_f32 v[126:127], v[126:127], 1.0 op_sel_hi:[1,0]
	v_cvt_f32_i32_e32 v116, v116
	v_rcp_f32_e32 v126, v126
	v_rcp_f32_e32 v127, v127
	s_nop 0
	v_pk_mul_f32 v[118:119], v[118:119], v[126:127]
	s_nop 0
	v_pk_mul_f32 v[114:115], v[114:115], v[118:119]
	v_pk_mul_f32 v[118:119], v[72:73], v[158:159] op_sel_hi:[1,0]
	v_pk_mul_f32 v[126:127], v[76:77], v[158:159] op_sel_hi:[1,0]
	v_pk_fma_f32 v[118:119], v[120:121], v[118:119], v[84:85]
	v_pk_fma_f32 v[116:117], v[116:117], v[126:127], v[80:81]
	v_min_f32_e32 v118, 0x40e00000, v118
	v_min_f32_e32 v119, 0x40e00000, v119
	v_pk_mul_f32 v[120:121], v[118:119], s[30:31] op_sel_hi:[1,0]
	v_med3_f32 v116, v116, s69, v193
	v_exp_f32_e32 v120, v120
	v_exp_f32_e32 v121, v121
	v_med3_f32 v117, v117, s69, v193
	v_pk_add_f32 v[116:117], v[116:117], 1.0 op_sel_hi:[1,0]
	v_max_f32_e64 v128, |v114|, |v115|
	v_pk_add_f32 v[120:121], v[120:121], 1.0 op_sel_hi:[1,0]
	s_nop 0
	v_rcp_f32_e32 v120, v120
	v_rcp_f32_e32 v121, v121
	s_nop 0
	v_pk_mul_f32 v[118:119], v[118:119], v[120:121]
	s_nop 0
	v_pk_mul_f32 v[118:119], v[116:117], v[118:119]
	s_nop 0
	v_max_f32_e64 v116, |v118|, |v119|
	v_max3_f32 v0, v0, v128, v116
	v_mov_b32_e32 v117, v0
	s_nop 1
	v_permlane16_swap_b32_e32 v0, v117
	v_max_f32_e32 v0, v0, v117
	v_mov_b32_e32 v117, v0
	s_nop 1
	v_permlane32_swap_b32_e32 v0, v117
	v_or_b32_e32 v116, 32, v178
	v_max_f32_e32 v120, v0, v117
	v_ashrrev_i32_e32 v117, 31, v116
	s_and_saveexec_b64 s[40:41], s[4:5]
	s_cbranch_execz .LBB0_1225
	s_lshl_b32 s42, s10, 2
	v_lshlrev_b64 v[126:127], 8, v[116:117]
	s_ashr_i32 s43, s42, 31
	v_lshl_add_u64 v[126:127], s[12:13], 0, v[126:127]
	v_lshl_add_u64 v[126:127], s[42:43], 2, v[126:127]
	s_lshl_b32 s16, s62, 2
	v_lshl_add_u64 v[126:127], v[126:127], 0, s[16:17]
	global_store_dword v[126:127], v120, off
.LBB0_1225:
	s_or_b64 exec, exec, s[40:41]
	v_rcp_f32_e32 v0, v120
	v_cmp_lt_f32_e32 vcc, 0, v120
	v_cvt_f32_i32_e32 v111, v111
	v_cvt_f32_i32_e32 v110, v110
	v_mul_f32_e32 v0, 0x42fe0000, v0
	v_cndmask_b32_e32 v0, 0, v0, vcc
	v_pk_mul_f32 v[120:121], v[122:123], v[0:1] op_sel_hi:[1,0]
	v_pk_mul_f32 v[122:123], v[124:125], v[0:1] op_sel_hi:[1,0]
	v_pk_mul_f32 v[114:115], v[114:115], v[0:1] op_sel_hi:[1,0]
	v_pk_mul_f32 v[118:119], v[118:119], v[0:1] op_sel_hi:[1,0]
	v_add_f32_e32 v0, 0x4b400000, v120
	v_add_f32_e32 v120, 0x4b400000, v121
	v_add_f32_e32 v121, 0x4b400000, v122
	v_add_f32_e32 v122, 0x4b400000, v123
	v_perm_b32 v0, v120, v0, s70
	v_perm_b32 v120, v122, v121, s70
	v_lshl_or_b32 v120, v120, 16, v0
	v_add_f32_e32 v0, 0x4b400000, v114
	v_add_f32_e32 v114, 0x4b400000, v115
	v_add_f32_e32 v115, 0x4b400000, v118
	v_add_f32_e32 v118, 0x4b400000, v119
	v_perm_b32 v0, v114, v0, s70
	v_perm_b32 v114, v118, v115, s70
	v_lshl_or_b32 v121, v114, 16, v0
	v_lshlrev_b64 v[114:115], 11, v[116:117]
	v_lshl_add_u64 v[114:115], s[2:3], 0, v[114:115]
	v_lshl_add_u64 v[114:115], v[114:115], 0, v[176:177]
	global_store_dwordx2 v[114:115], v[120:121], off
	v_pk_mul_f32 v[114:115], v[98:99], v[156:157] op_sel_hi:[1,0]
	v_cvt_f32_i32_e32 v91, v91
	v_pk_fma_f32 v[110:111], v[110:111], v[114:115], v[106:107]
	v_cvt_f32_i32_e32 v90, v90
	v_min_f32_e32 v110, 0x40e00000, v110
	v_min_f32_e32 v111, 0x40e00000, v111
	v_pk_mul_f32 v[114:115], v[110:111], s[30:31] op_sel_hi:[1,0]
	v_pk_mul_f32 v[116:117], v[102:103], v[156:157] op_sel_hi:[1,0]
	v_exp_f32_e32 v114, v114
	v_exp_f32_e32 v115, v115
	v_pk_fma_f32 v[90:91], v[90:91], v[116:117], v[94:95]
	v_cvt_f32_i32_e32 v113, v113
	v_cvt_f32_i32_e32 v112, v112
	v_pk_add_f32 v[114:115], v[114:115], 1.0 op_sel_hi:[1,0]
	v_med3_f32 v90, v90, s69, v193
	v_rcp_f32_e32 v114, v114
	v_rcp_f32_e32 v115, v115
	v_med3_f32 v91, v91, s69, v193
	v_pk_add_f32 v[90:91], v[90:91], 1.0 op_sel_hi:[1,0]
	v_cvt_f32_i32_e32 v93, v93
	v_pk_mul_f32 v[110:111], v[110:111], v[114:115]
	v_cvt_f32_i32_e32 v92, v92
	v_pk_mul_f32 v[90:91], v[90:91], v[110:111]
	v_pk_mul_f32 v[110:111], v[100:101], v[156:157] op_sel_hi:[1,0]
	v_pk_mul_f32 v[114:115], v[104:105], v[156:157] op_sel_hi:[1,0]
	v_pk_fma_f32 v[110:111], v[112:113], v[110:111], v[108:109]
	v_pk_fma_f32 v[92:93], v[92:93], v[114:115], v[96:97]
	v_min_f32_e32 v110, 0x40e00000, v110
	v_min_f32_e32 v111, 0x40e00000, v111
	v_pk_mul_f32 v[112:113], v[110:111], s[30:31] op_sel_hi:[1,0]
	v_med3_f32 v92, v92, s69, v193
	v_exp_f32_e32 v112, v112
	v_exp_f32_e32 v113, v113
	v_med3_f32 v93, v93, s69, v193
	v_pk_add_f32 v[92:93], v[92:93], 1.0 op_sel_hi:[1,0]
	v_cvt_f32_i32_e32 v87, v87
	v_pk_add_f32 v[112:113], v[112:113], 1.0 op_sel_hi:[1,0]
	v_cvt_f32_i32_e32 v86, v86
	v_rcp_f32_e32 v112, v112
	v_rcp_f32_e32 v113, v113
	v_max_f32_e64 v0, |v90|, |v91|
	v_cvt_f32_i32_e32 v67, v67
	v_cvt_f32_i32_e32 v66, v66
	v_pk_mul_f32 v[110:111], v[110:111], v[112:113]
	v_pk_mul_f32 v[112:113], v[74:75], v[156:157] op_sel_hi:[1,0]
	v_pk_mul_f32 v[92:93], v[92:93], v[110:111]
	v_pk_fma_f32 v[66:67], v[66:67], v[112:113], v[78:79]
	v_max_f32_e64 v110, |v92|, |v93|
	v_max3_f32 v0, v0, 0, v110
	v_pk_mul_f32 v[110:111], v[70:71], v[156:157] op_sel_hi:[1,0]
	v_cvt_f32_i32_e32 v89, v89
	v_pk_fma_f32 v[86:87], v[86:87], v[110:111], v[82:83]
	v_cvt_f32_i32_e32 v88, v88
	v_min_f32_e32 v86, 0x40e00000, v86
	v_min_f32_e32 v87, 0x40e00000, v87
	v_pk_mul_f32 v[110:111], v[86:87], s[30:31] op_sel_hi:[1,0]
	v_med3_f32 v66, v66, s69, v193
	v_exp_f32_e32 v110, v110
	v_exp_f32_e32 v111, v111
	v_med3_f32 v67, v67, s69, v193
	v_pk_add_f32 v[66:67], v[66:67], 1.0 op_sel_hi:[1,0]
	v_cvt_f32_i32_e32 v69, v69
	v_pk_add_f32 v[110:111], v[110:111], 1.0 op_sel_hi:[1,0]
	v_cvt_f32_i32_e32 v68, v68
	v_rcp_f32_e32 v110, v110
	v_rcp_f32_e32 v111, v111
	s_nop 0
	v_pk_mul_f32 v[86:87], v[86:87], v[110:111]
	s_nop 0
	v_pk_mul_f32 v[86:87], v[66:67], v[86:87]
	v_pk_mul_f32 v[66:67], v[72:73], v[156:157] op_sel_hi:[1,0]
	v_pk_mul_f32 v[110:111], v[76:77], v[156:157] op_sel_hi:[1,0]
	v_pk_fma_f32 v[66:67], v[88:89], v[66:67], v[84:85]
	v_pk_fma_f32 v[68:69], v[68:69], v[110:111], v[80:81]
	v_min_f32_e32 v66, 0x40e00000, v66
	v_min_f32_e32 v67, 0x40e00000, v67
	v_pk_mul_f32 v[88:89], v[66:67], s[30:31] op_sel_hi:[1,0]
	v_med3_f32 v68, v68, s69, v193
	v_exp_f32_e32 v88, v88
	v_exp_f32_e32 v89, v89
	v_med3_f32 v69, v69, s69, v193
	v_pk_add_f32 v[68:69], v[68:69], 1.0 op_sel_hi:[1,0]
	v_max_f32_e64 v112, |v86|, |v87|
	v_pk_add_f32 v[88:89], v[88:89], 1.0 op_sel_hi:[1,0]
	s_nop 0
	v_rcp_f32_e32 v88, v88
	v_rcp_f32_e32 v89, v89
	s_nop 0
	v_pk_mul_f32 v[66:67], v[66:67], v[88:89]
	s_nop 0
	v_pk_mul_f32 v[88:89], v[68:69], v[66:67]
	v_or_b32_e32 v68, 48, v178
	v_max_f32_e64 v66, |v88|, |v89|
	v_max3_f32 v0, v0, v112, v66
	v_mov_b32_e32 v66, v0
	s_nop 1
	v_permlane16_swap_b32_e32 v0, v66
	v_max_f32_e32 v0, v0, v66
	v_mov_b32_e32 v66, v0
	s_nop 1
	v_permlane32_swap_b32_e32 v0, v66
	v_max_f32_e32 v110, v0, v66
	v_ashrrev_i32_e32 v69, 31, v68
	s_and_saveexec_b64 s[40:41], s[4:5]
	s_cbranch_execz .LBB0_1227
	s_lshl_b32 s42, s10, 2
	v_lshlrev_b64 v[66:67], 8, v[68:69]
	s_ashr_i32 s43, s42, 31
	v_lshl_add_u64 v[66:67], s[12:13], 0, v[66:67]
	v_lshl_add_u64 v[66:67], s[42:43], 2, v[66:67]
	s_lshl_b32 s16, s62, 2
	v_lshl_add_u64 v[66:67], v[66:67], 0, s[16:17]
	global_store_dword v[66:67], v110, off
.LBB0_1227:
	s_or_b64 exec, exec, s[40:41]
	v_rcp_f32_e32 v0, v110
	v_cmp_lt_f32_e32 vcc, 0, v110
	v_lshlrev_b64 v[68:69], 11, v[68:69]
	v_cvt_f32_i32_e32 v63, v63
	v_mul_f32_e32 v0, 0x42fe0000, v0
	v_cndmask_b32_e32 v0, 0, v0, vcc
	v_pk_mul_f32 v[90:91], v[90:91], v[0:1] op_sel_hi:[1,0]
	v_pk_mul_f32 v[92:93], v[92:93], v[0:1] op_sel_hi:[1,0]
	v_pk_mul_f32 v[86:87], v[86:87], v[0:1] op_sel_hi:[1,0]
	v_pk_mul_f32 v[88:89], v[88:89], v[0:1] op_sel_hi:[1,0]
	v_add_f32_e32 v0, 0x4b400000, v90
	v_add_f32_e32 v90, 0x4b400000, v91
	v_add_f32_e32 v91, 0x4b400000, v92
	v_add_f32_e32 v92, 0x4b400000, v93
	v_perm_b32 v0, v90, v0, s70
	v_perm_b32 v90, v92, v91, s70
	v_lshl_or_b32 v90, v90, 16, v0
	v_add_f32_e32 v0, 0x4b400000, v86
	v_add_f32_e32 v86, 0x4b400000, v87
	v_add_f32_e32 v87, 0x4b400000, v88
	v_add_f32_e32 v88, 0x4b400000, v89
	v_cvt_f32_i32_e32 v62, v62
	v_perm_b32 v0, v86, v0, s70
	v_perm_b32 v86, v88, v87, s70
	v_lshl_add_u64 v[68:69], s[2:3], 0, v[68:69]
	v_lshl_or_b32 v91, v86, 16, v0
	v_lshl_add_u64 v[68:69], v[68:69], 0, v[176:177]
	global_store_dwordx2 v[68:69], v[90:91], off
	v_pk_mul_f32 v[68:69], v[98:99], v[154:155] op_sel_hi:[1,0]
	v_cvt_f32_i32_e32 v59, v59
	v_pk_fma_f32 v[62:63], v[62:63], v[68:69], v[106:107]
	v_cvt_f32_i32_e32 v58, v58
	v_min_f32_e32 v62, 0x40e00000, v62
	v_min_f32_e32 v63, 0x40e00000, v63
	v_pk_mul_f32 v[68:69], v[62:63], s[30:31] op_sel_hi:[1,0]
	v_pk_mul_f32 v[86:87], v[102:103], v[154:155] op_sel_hi:[1,0]
	v_exp_f32_e32 v68, v68
	v_exp_f32_e32 v69, v69
	v_pk_fma_f32 v[58:59], v[58:59], v[86:87], v[94:95]
	v_cvt_f32_i32_e32 v65, v65
	v_cvt_f32_i32_e32 v64, v64
	v_pk_add_f32 v[68:69], v[68:69], 1.0 op_sel_hi:[1,0]
	v_med3_f32 v58, v58, s69, v193
	v_rcp_f32_e32 v68, v68
	v_rcp_f32_e32 v69, v69
	v_med3_f32 v59, v59, s69, v193
	v_pk_add_f32 v[58:59], v[58:59], 1.0 op_sel_hi:[1,0]
	v_cvt_f32_i32_e32 v61, v61
	v_pk_mul_f32 v[62:63], v[62:63], v[68:69]
	v_cvt_f32_i32_e32 v60, v60
	v_pk_mul_f32 v[58:59], v[58:59], v[62:63]
	v_pk_mul_f32 v[62:63], v[100:101], v[154:155] op_sel_hi:[1,0]
	v_pk_mul_f32 v[68:69], v[104:105], v[154:155] op_sel_hi:[1,0]
	v_pk_fma_f32 v[62:63], v[64:65], v[62:63], v[108:109]
	v_pk_fma_f32 v[60:61], v[60:61], v[68:69], v[96:97]
	v_min_f32_e32 v62, 0x40e00000, v62
	v_min_f32_e32 v63, 0x40e00000, v63
	v_pk_mul_f32 v[64:65], v[62:63], s[30:31] op_sel_hi:[1,0]
	v_med3_f32 v60, v60, s69, v193
	v_exp_f32_e32 v64, v64
	v_exp_f32_e32 v65, v65
	v_med3_f32 v61, v61, s69, v193
	v_pk_add_f32 v[60:61], v[60:61], 1.0 op_sel_hi:[1,0]
	v_cvt_f32_i32_e32 v55, v55
	v_pk_add_f32 v[64:65], v[64:65], 1.0 op_sel_hi:[1,0]
	v_cvt_f32_i32_e32 v54, v54
	v_rcp_f32_e32 v64, v64
	v_rcp_f32_e32 v65, v65
	v_max_f32_e64 v0, |v58|, |v59|
	v_cvt_f32_i32_e32 v51, v51
	v_cvt_f32_i32_e32 v50, v50
	v_pk_mul_f32 v[62:63], v[62:63], v[64:65]
	v_pk_mul_f32 v[64:65], v[74:75], v[154:155] op_sel_hi:[1,0]
	v_pk_mul_f32 v[60:61], v[60:61], v[62:63]
	v_pk_fma_f32 v[50:51], v[50:51], v[64:65], v[78:79]
	v_max_f32_e64 v62, |v60|, |v61|
	v_max3_f32 v0, v0, 0, v62
	v_pk_mul_f32 v[62:63], v[70:71], v[154:155] op_sel_hi:[1,0]
	v_cvt_f32_i32_e32 v57, v57
	v_pk_fma_f32 v[54:55], v[54:55], v[62:63], v[82:83]
	v_cvt_f32_i32_e32 v56, v56
	v_min_f32_e32 v54, 0x40e00000, v54
	v_min_f32_e32 v55, 0x40e00000, v55
	v_pk_mul_f32 v[62:63], v[54:55], s[30:31] op_sel_hi:[1,0]
	v_med3_f32 v50, v50, s69, v193
	v_exp_f32_e32 v62, v62
	v_exp_f32_e32 v63, v63
	v_med3_f32 v51, v51, s69, v193
	v_pk_add_f32 v[50:51], v[50:51], 1.0 op_sel_hi:[1,0]
	v_cvt_f32_i32_e32 v53, v53
	v_pk_add_f32 v[62:63], v[62:63], 1.0 op_sel_hi:[1,0]
	v_cvt_f32_i32_e32 v52, v52
	v_rcp_f32_e32 v62, v62
	v_rcp_f32_e32 v63, v63
	v_add_u32_e32 v66, 0x80, v178
	v_ashrrev_i32_e32 v67, 31, v66
	v_pk_mul_f32 v[54:55], v[54:55], v[62:63]
	s_nop 0
	v_pk_mul_f32 v[50:51], v[50:51], v[54:55]
	v_pk_mul_f32 v[54:55], v[72:73], v[154:155] op_sel_hi:[1,0]
	v_pk_mul_f32 v[62:63], v[76:77], v[154:155] op_sel_hi:[1,0]
	v_pk_fma_f32 v[54:55], v[56:57], v[54:55], v[84:85]
	v_pk_fma_f32 v[52:53], v[52:53], v[62:63], v[80:81]
	v_min_f32_e32 v54, 0x40e00000, v54
	v_min_f32_e32 v55, 0x40e00000, v55
	v_pk_mul_f32 v[56:57], v[54:55], s[30:31] op_sel_hi:[1,0]
	v_med3_f32 v52, v52, s69, v193
	v_exp_f32_e32 v56, v56
	v_exp_f32_e32 v57, v57
	v_med3_f32 v53, v53, s69, v193
	v_pk_add_f32 v[52:53], v[52:53], 1.0 op_sel_hi:[1,0]
	v_max_f32_e64 v64, |v50|, |v51|
	v_pk_add_f32 v[56:57], v[56:57], 1.0 op_sel_hi:[1,0]
	s_nop 0
	v_rcp_f32_e32 v56, v56
	v_rcp_f32_e32 v57, v57
	s_nop 0
	v_pk_mul_f32 v[54:55], v[54:55], v[56:57]
	s_nop 0
	v_pk_mul_f32 v[52:53], v[52:53], v[54:55]
	s_nop 0
	v_max_f32_e64 v54, |v52|, |v53|
	v_max3_f32 v0, v0, v64, v54
	v_mov_b32_e32 v54, v0
	s_nop 1
	v_permlane16_swap_b32_e32 v0, v54
	v_max_f32_e32 v0, v0, v54
	v_mov_b32_e32 v54, v0
	s_nop 1
	v_permlane32_swap_b32_e32 v0, v54
	v_max_f32_e32 v54, v0, v54
	s_and_saveexec_b64 s[40:41], s[4:5]
	s_cbranch_execz .LBB0_1229
	v_lshlrev_b64 v[56:57], 8, v[66:67]
	s_lshl_b32 s42, s10, 2
	v_lshl_add_u64 v[56:57], s[12:13], 0, v[56:57]
	s_ashr_i32 s43, s42, 31
	v_lshl_add_u64 v[56:57], s[42:43], 2, v[56:57]
	s_lshl_b32 s16, s62, 2
	v_lshl_add_u64 v[56:57], v[56:57], 0, s[16:17]
	global_store_dword v[56:57], v54, off
.LBB0_1229:
	s_or_b64 exec, exec, s[40:41]
	v_rcp_f32_e32 v0, v54
	v_cmp_lt_f32_e32 vcc, 0, v54
	v_cvt_f32_i32_e32 v47, v47
	v_cvt_f32_i32_e32 v46, v46
	v_mul_f32_e32 v0, 0x42fe0000, v0
	v_cndmask_b32_e32 v0, 0, v0, vcc
	v_pk_mul_f32 v[54:55], v[58:59], v[0:1] op_sel_hi:[1,0]
	v_pk_mul_f32 v[56:57], v[60:61], v[0:1] op_sel_hi:[1,0]
	v_pk_mul_f32 v[50:51], v[50:51], v[0:1] op_sel_hi:[1,0]
	v_pk_mul_f32 v[52:53], v[52:53], v[0:1] op_sel_hi:[1,0]
	v_add_f32_e32 v0, 0x4b400000, v54
	v_add_f32_e32 v54, 0x4b400000, v55
	v_add_f32_e32 v55, 0x4b400000, v56
	v_add_f32_e32 v56, 0x4b400000, v57
	v_perm_b32 v0, v54, v0, s70
	v_perm_b32 v54, v56, v55, s70
	v_lshl_or_b32 v54, v54, 16, v0
	v_add_f32_e32 v0, 0x4b400000, v50
	v_add_f32_e32 v50, 0x4b400000, v51
	v_add_f32_e32 v51, 0x4b400000, v52
	v_add_f32_e32 v52, 0x4b400000, v53
	v_perm_b32 v0, v50, v0, s70
	v_perm_b32 v50, v52, v51, s70
	v_lshl_or_b32 v55, v50, 16, v0
	v_lshlrev_b64 v[50:51], 11, v[66:67]
	v_lshl_add_u64 v[50:51], s[2:3], 0, v[50:51]
	v_lshl_add_u64 v[50:51], v[50:51], 0, v[176:177]
	global_store_dwordx2 v[50:51], v[54:55], off
	v_pk_mul_f32 v[50:51], v[98:99], v[152:153] op_sel_hi:[1,0]
	v_cvt_f32_i32_e32 v43, v43
	v_pk_fma_f32 v[46:47], v[46:47], v[50:51], v[106:107]
	v_cvt_f32_i32_e32 v42, v42
	v_min_f32_e32 v46, 0x40e00000, v46
	v_min_f32_e32 v47, 0x40e00000, v47
	v_pk_mul_f32 v[50:51], v[46:47], s[30:31] op_sel_hi:[1,0]
	v_pk_mul_f32 v[52:53], v[102:103], v[152:153] op_sel_hi:[1,0]
	v_exp_f32_e32 v50, v50
	v_exp_f32_e32 v51, v51
	v_pk_fma_f32 v[42:43], v[42:43], v[52:53], v[94:95]
	v_cvt_f32_i32_e32 v49, v49
	v_cvt_f32_i32_e32 v48, v48
	v_pk_add_f32 v[50:51], v[50:51], 1.0 op_sel_hi:[1,0]
	v_med3_f32 v42, v42, s69, v193
	v_rcp_f32_e32 v50, v50
	v_rcp_f32_e32 v51, v51
	v_med3_f32 v43, v43, s69, v193
	v_pk_add_f32 v[42:43], v[42:43], 1.0 op_sel_hi:[1,0]
	v_cvt_f32_i32_e32 v45, v45
	v_pk_mul_f32 v[46:47], v[46:47], v[50:51]
	v_cvt_f32_i32_e32 v44, v44
	v_pk_mul_f32 v[42:43], v[42:43], v[46:47]
	v_pk_mul_f32 v[46:47], v[100:101], v[152:153] op_sel_hi:[1,0]
	v_pk_mul_f32 v[50:51], v[104:105], v[152:153] op_sel_hi:[1,0]
	v_pk_fma_f32 v[46:47], v[48:49], v[46:47], v[108:109]
	v_pk_fma_f32 v[44:45], v[44:45], v[50:51], v[96:97]
	v_min_f32_e32 v46, 0x40e00000, v46
	v_min_f32_e32 v47, 0x40e00000, v47
	v_pk_mul_f32 v[48:49], v[46:47], s[30:31] op_sel_hi:[1,0]
	v_med3_f32 v44, v44, s69, v193
	v_exp_f32_e32 v48, v48
	v_exp_f32_e32 v49, v49
	v_med3_f32 v45, v45, s69, v193
	v_pk_add_f32 v[44:45], v[44:45], 1.0 op_sel_hi:[1,0]
	v_cvt_f32_i32_e32 v39, v39
	v_pk_add_f32 v[48:49], v[48:49], 1.0 op_sel_hi:[1,0]
	v_cvt_f32_i32_e32 v38, v38
	v_rcp_f32_e32 v48, v48
	v_rcp_f32_e32 v49, v49
	v_max_f32_e64 v0, |v42|, |v43|
	v_cvt_f32_i32_e32 v35, v35
	v_cvt_f32_i32_e32 v34, v34
	v_pk_mul_f32 v[46:47], v[46:47], v[48:49]
	v_pk_mul_f32 v[48:49], v[74:75], v[152:153] op_sel_hi:[1,0]
	v_pk_mul_f32 v[44:45], v[44:45], v[46:47]
	v_pk_fma_f32 v[34:35], v[34:35], v[48:49], v[78:79]
	v_max_f32_e64 v46, |v44|, |v45|
	v_max3_f32 v0, v0, 0, v46
	v_pk_mul_f32 v[46:47], v[70:71], v[152:153] op_sel_hi:[1,0]
	v_cvt_f32_i32_e32 v41, v41
	v_pk_fma_f32 v[38:39], v[38:39], v[46:47], v[82:83]
	v_cvt_f32_i32_e32 v40, v40
	v_min_f32_e32 v38, 0x40e00000, v38
	v_min_f32_e32 v39, 0x40e00000, v39
	v_pk_mul_f32 v[46:47], v[38:39], s[30:31] op_sel_hi:[1,0]
	v_med3_f32 v34, v34, s69, v193
	v_exp_f32_e32 v46, v46
	v_exp_f32_e32 v47, v47
	v_med3_f32 v35, v35, s69, v193
	v_pk_add_f32 v[34:35], v[34:35], 1.0 op_sel_hi:[1,0]
	v_cvt_f32_i32_e32 v37, v37
	v_pk_add_f32 v[46:47], v[46:47], 1.0 op_sel_hi:[1,0]
	v_cvt_f32_i32_e32 v36, v36
	v_rcp_f32_e32 v46, v46
	v_rcp_f32_e32 v47, v47
	s_nop 0
	v_pk_mul_f32 v[38:39], v[38:39], v[46:47]
	s_nop 0
	v_pk_mul_f32 v[34:35], v[34:35], v[38:39]
	v_pk_mul_f32 v[38:39], v[72:73], v[152:153] op_sel_hi:[1,0]
	v_pk_mul_f32 v[46:47], v[76:77], v[152:153] op_sel_hi:[1,0]
	v_pk_fma_f32 v[38:39], v[40:41], v[38:39], v[84:85]
	v_pk_fma_f32 v[36:37], v[36:37], v[46:47], v[80:81]
	v_min_f32_e32 v38, 0x40e00000, v38
	v_min_f32_e32 v39, 0x40e00000, v39
	v_pk_mul_f32 v[40:41], v[38:39], s[30:31] op_sel_hi:[1,0]
	v_med3_f32 v36, v36, s69, v193
	v_exp_f32_e32 v40, v40
	v_exp_f32_e32 v41, v41
	v_med3_f32 v37, v37, s69, v193
	v_pk_add_f32 v[36:37], v[36:37], 1.0 op_sel_hi:[1,0]
	v_max_f32_e64 v48, |v34|, |v35|
	v_pk_add_f32 v[40:41], v[40:41], 1.0 op_sel_hi:[1,0]
	s_nop 0
	v_rcp_f32_e32 v40, v40
	v_rcp_f32_e32 v41, v41
	s_nop 0
	v_pk_mul_f32 v[38:39], v[38:39], v[40:41]
	s_nop 0
	v_pk_mul_f32 v[38:39], v[36:37], v[38:39]
	s_nop 0
	v_max_f32_e64 v36, |v38|, |v39|
	v_max3_f32 v0, v0, v48, v36
	v_mov_b32_e32 v37, v0
	s_nop 1
	v_permlane16_swap_b32_e32 v0, v37
	v_max_f32_e32 v0, v0, v37
	v_mov_b32_e32 v37, v0
	s_nop 1
	v_permlane32_swap_b32_e32 v0, v37
	v_add_u32_e32 v36, 0x90, v178
	v_max_f32_e32 v40, v0, v37
	v_ashrrev_i32_e32 v37, 31, v36
	s_and_saveexec_b64 s[40:41], s[4:5]
	s_cbranch_execz .LBB0_1231
	s_lshl_b32 s42, s10, 2
	v_lshlrev_b64 v[46:47], 8, v[36:37]
	s_ashr_i32 s43, s42, 31
	v_lshl_add_u64 v[46:47], s[12:13], 0, v[46:47]
	v_lshl_add_u64 v[46:47], s[42:43], 2, v[46:47]
	s_lshl_b32 s16, s62, 2
	v_lshl_add_u64 v[46:47], v[46:47], 0, s[16:17]
	global_store_dword v[46:47], v40, off
.LBB0_1231:
	s_or_b64 exec, exec, s[40:41]
	v_rcp_f32_e32 v0, v40
	v_cmp_lt_f32_e32 vcc, 0, v40
	v_cvt_f32_i32_e32 v31, v31
	v_cvt_f32_i32_e32 v30, v30
	v_mul_f32_e32 v0, 0x42fe0000, v0
	v_cndmask_b32_e32 v0, 0, v0, vcc
	v_pk_mul_f32 v[40:41], v[42:43], v[0:1] op_sel_hi:[1,0]
	v_pk_mul_f32 v[42:43], v[44:45], v[0:1] op_sel_hi:[1,0]
	v_pk_mul_f32 v[34:35], v[34:35], v[0:1] op_sel_hi:[1,0]
	v_pk_mul_f32 v[38:39], v[38:39], v[0:1] op_sel_hi:[1,0]
	v_add_f32_e32 v0, 0x4b400000, v40
	v_add_f32_e32 v40, 0x4b400000, v41
	v_add_f32_e32 v41, 0x4b400000, v42
	v_add_f32_e32 v42, 0x4b400000, v43
	v_perm_b32 v0, v40, v0, s70
	v_perm_b32 v40, v42, v41, s70
	v_lshl_or_b32 v40, v40, 16, v0
	v_add_f32_e32 v0, 0x4b400000, v34
	v_add_f32_e32 v34, 0x4b400000, v35
	v_add_f32_e32 v35, 0x4b400000, v38
	v_add_f32_e32 v38, 0x4b400000, v39
	v_perm_b32 v0, v34, v0, s70
	v_perm_b32 v34, v38, v35, s70
	v_lshl_or_b32 v41, v34, 16, v0
	v_lshlrev_b64 v[34:35], 11, v[36:37]
	v_lshl_add_u64 v[34:35], s[2:3], 0, v[34:35]
	v_lshl_add_u64 v[34:35], v[34:35], 0, v[176:177]
	global_store_dwordx2 v[34:35], v[40:41], off
	v_pk_mul_f32 v[34:35], v[98:99], v[150:151] op_sel_hi:[1,0]
	v_cvt_f32_i32_e32 v27, v27
	v_pk_fma_f32 v[30:31], v[30:31], v[34:35], v[106:107]
	v_cvt_f32_i32_e32 v26, v26
	v_min_f32_e32 v30, 0x40e00000, v30
	v_min_f32_e32 v31, 0x40e00000, v31
	v_pk_mul_f32 v[34:35], v[30:31], s[30:31] op_sel_hi:[1,0]
	v_pk_mul_f32 v[36:37], v[102:103], v[150:151] op_sel_hi:[1,0]
	v_exp_f32_e32 v34, v34
	v_exp_f32_e32 v35, v35
	v_pk_fma_f32 v[26:27], v[26:27], v[36:37], v[94:95]
	v_cvt_f32_i32_e32 v33, v33
	v_cvt_f32_i32_e32 v32, v32
	v_pk_add_f32 v[34:35], v[34:35], 1.0 op_sel_hi:[1,0]
	v_med3_f32 v26, v26, s69, v193
	v_rcp_f32_e32 v34, v34
	v_rcp_f32_e32 v35, v35
	v_med3_f32 v27, v27, s69, v193
	v_pk_add_f32 v[26:27], v[26:27], 1.0 op_sel_hi:[1,0]
	v_cvt_f32_i32_e32 v29, v29
	v_pk_mul_f32 v[30:31], v[30:31], v[34:35]
	v_cvt_f32_i32_e32 v28, v28
	v_pk_mul_f32 v[26:27], v[26:27], v[30:31]
	v_pk_mul_f32 v[30:31], v[100:101], v[150:151] op_sel_hi:[1,0]
	v_pk_mul_f32 v[34:35], v[104:105], v[150:151] op_sel_hi:[1,0]
	v_pk_fma_f32 v[30:31], v[32:33], v[30:31], v[108:109]
	v_pk_fma_f32 v[28:29], v[28:29], v[34:35], v[96:97]
	v_min_f32_e32 v30, 0x40e00000, v30
	v_min_f32_e32 v31, 0x40e00000, v31
	v_pk_mul_f32 v[32:33], v[30:31], s[30:31] op_sel_hi:[1,0]
	v_med3_f32 v28, v28, s69, v193
	v_exp_f32_e32 v32, v32
	v_exp_f32_e32 v33, v33
	v_med3_f32 v29, v29, s69, v193
	v_pk_add_f32 v[28:29], v[28:29], 1.0 op_sel_hi:[1,0]
	v_cvt_f32_i32_e32 v23, v23
	v_pk_add_f32 v[32:33], v[32:33], 1.0 op_sel_hi:[1,0]
	v_cvt_f32_i32_e32 v22, v22
	v_rcp_f32_e32 v32, v32
	v_rcp_f32_e32 v33, v33
	v_max_f32_e64 v0, |v26|, |v27|
	v_cvt_f32_i32_e32 v19, v19
	v_cvt_f32_i32_e32 v18, v18
	v_pk_mul_f32 v[30:31], v[30:31], v[32:33]
	v_pk_mul_f32 v[32:33], v[74:75], v[150:151] op_sel_hi:[1,0]
	v_pk_mul_f32 v[28:29], v[28:29], v[30:31]
	v_pk_fma_f32 v[18:19], v[18:19], v[32:33], v[78:79]
	v_max_f32_e64 v30, |v28|, |v29|
	v_max3_f32 v0, v0, 0, v30
	v_pk_mul_f32 v[30:31], v[70:71], v[150:151] op_sel_hi:[1,0]
	v_cvt_f32_i32_e32 v25, v25
	v_pk_fma_f32 v[22:23], v[22:23], v[30:31], v[82:83]
	v_cvt_f32_i32_e32 v24, v24
	v_min_f32_e32 v22, 0x40e00000, v22
	v_min_f32_e32 v23, 0x40e00000, v23
	v_pk_mul_f32 v[30:31], v[22:23], s[30:31] op_sel_hi:[1,0]
	v_med3_f32 v18, v18, s69, v193
	v_exp_f32_e32 v30, v30
	v_exp_f32_e32 v31, v31
	v_med3_f32 v19, v19, s69, v193
	v_pk_add_f32 v[18:19], v[18:19], 1.0 op_sel_hi:[1,0]
	v_cvt_f32_i32_e32 v21, v21
	v_pk_add_f32 v[30:31], v[30:31], 1.0 op_sel_hi:[1,0]
	v_cvt_f32_i32_e32 v20, v20
	v_rcp_f32_e32 v30, v30
	v_rcp_f32_e32 v31, v31
	s_nop 0
	v_pk_mul_f32 v[22:23], v[22:23], v[30:31]
	s_nop 0
	v_pk_mul_f32 v[18:19], v[18:19], v[22:23]
	v_pk_mul_f32 v[22:23], v[72:73], v[150:151] op_sel_hi:[1,0]
	v_pk_mul_f32 v[30:31], v[76:77], v[150:151] op_sel_hi:[1,0]
	v_pk_fma_f32 v[22:23], v[24:25], v[22:23], v[84:85]
	v_pk_fma_f32 v[20:21], v[20:21], v[30:31], v[80:81]
	v_min_f32_e32 v22, 0x40e00000, v22
	v_min_f32_e32 v23, 0x40e00000, v23
	v_pk_mul_f32 v[24:25], v[22:23], s[30:31] op_sel_hi:[1,0]
	v_med3_f32 v20, v20, s69, v193
	v_exp_f32_e32 v24, v24
	v_exp_f32_e32 v25, v25
	v_med3_f32 v21, v21, s69, v193
	v_pk_add_f32 v[20:21], v[20:21], 1.0 op_sel_hi:[1,0]
	v_max_f32_e64 v32, |v18|, |v19|
	v_pk_add_f32 v[24:25], v[24:25], 1.0 op_sel_hi:[1,0]
	s_nop 0
	v_rcp_f32_e32 v24, v24
	v_rcp_f32_e32 v25, v25
	s_nop 0
	v_pk_mul_f32 v[22:23], v[22:23], v[24:25]
	s_nop 0
	v_pk_mul_f32 v[22:23], v[20:21], v[22:23]
	s_nop 0
	v_max_f32_e64 v20, |v22|, |v23|
	v_max3_f32 v0, v0, v32, v20
	v_mov_b32_e32 v21, v0
	s_nop 1
	v_permlane16_swap_b32_e32 v0, v21
	v_max_f32_e32 v0, v0, v21
	v_mov_b32_e32 v21, v0
	s_nop 1
	v_permlane32_swap_b32_e32 v0, v21
	v_add_u32_e32 v20, 0xa0, v178
	v_max_f32_e32 v24, v0, v21
	v_ashrrev_i32_e32 v21, 31, v20
	s_and_saveexec_b64 s[40:41], s[4:5]
	s_cbranch_execz .LBB0_1233
	s_lshl_b32 s42, s10, 2
	v_lshlrev_b64 v[30:31], 8, v[20:21]
	s_ashr_i32 s43, s42, 31
	v_lshl_add_u64 v[30:31], s[12:13], 0, v[30:31]
	v_lshl_add_u64 v[30:31], s[42:43], 2, v[30:31]
	s_lshl_b32 s16, s62, 2
	v_lshl_add_u64 v[30:31], v[30:31], 0, s[16:17]
	global_store_dword v[30:31], v24, off
.LBB0_1233:
	s_or_b64 exec, exec, s[40:41]
	v_rcp_f32_e32 v0, v24
	v_cmp_lt_f32_e32 vcc, 0, v24
	v_cvt_f32_i32_e32 v15, v15
	v_cvt_f32_i32_e32 v14, v14
	v_mul_f32_e32 v0, 0x42fe0000, v0
	v_cndmask_b32_e32 v0, 0, v0, vcc
	v_pk_mul_f32 v[24:25], v[26:27], v[0:1] op_sel_hi:[1,0]
	v_pk_mul_f32 v[26:27], v[28:29], v[0:1] op_sel_hi:[1,0]
	v_pk_mul_f32 v[18:19], v[18:19], v[0:1] op_sel_hi:[1,0]
	v_pk_mul_f32 v[22:23], v[22:23], v[0:1] op_sel_hi:[1,0]
	v_add_f32_e32 v0, 0x4b400000, v24
	v_add_f32_e32 v24, 0x4b400000, v25
	v_add_f32_e32 v25, 0x4b400000, v26
	v_add_f32_e32 v26, 0x4b400000, v27
	v_perm_b32 v0, v24, v0, s70
	v_perm_b32 v24, v26, v25, s70
	v_lshl_or_b32 v24, v24, 16, v0
	v_add_f32_e32 v0, 0x4b400000, v18
	v_add_f32_e32 v18, 0x4b400000, v19
	v_add_f32_e32 v19, 0x4b400000, v22
	v_add_f32_e32 v22, 0x4b400000, v23
	v_perm_b32 v0, v18, v0, s70
	v_perm_b32 v18, v22, v19, s70
	v_lshl_or_b32 v25, v18, 16, v0
	v_lshlrev_b64 v[18:19], 11, v[20:21]
	v_lshl_add_u64 v[18:19], s[2:3], 0, v[18:19]
	v_lshl_add_u64 v[18:19], v[18:19], 0, v[176:177]
	global_store_dwordx2 v[18:19], v[24:25], off
	v_pk_mul_f32 v[18:19], v[98:99], v[146:147] op_sel_hi:[1,0]
	v_cvt_f32_i32_e32 v11, v11
	v_pk_fma_f32 v[14:15], v[14:15], v[18:19], v[106:107]
	v_cvt_f32_i32_e32 v10, v10
	v_min_f32_e32 v14, 0x40e00000, v14
	v_min_f32_e32 v15, 0x40e00000, v15
	v_pk_mul_f32 v[18:19], v[14:15], s[30:31] op_sel_hi:[1,0]
	v_pk_mul_f32 v[20:21], v[102:103], v[146:147] op_sel_hi:[1,0]
	v_exp_f32_e32 v18, v18
	v_exp_f32_e32 v19, v19
	v_pk_fma_f32 v[10:11], v[10:11], v[20:21], v[94:95]
	v_cvt_f32_i32_e32 v17, v17
	v_cvt_f32_i32_e32 v16, v16
	v_pk_add_f32 v[18:19], v[18:19], 1.0 op_sel_hi:[1,0]
	v_med3_f32 v10, v10, s69, v193
	v_rcp_f32_e32 v18, v18
	v_rcp_f32_e32 v19, v19
	v_med3_f32 v11, v11, s69, v193
	v_pk_add_f32 v[10:11], v[10:11], 1.0 op_sel_hi:[1,0]
	v_cvt_f32_i32_e32 v13, v13
	v_pk_mul_f32 v[14:15], v[14:15], v[18:19]
	v_cvt_f32_i32_e32 v12, v12
	v_pk_mul_f32 v[10:11], v[10:11], v[14:15]
	v_pk_mul_f32 v[14:15], v[100:101], v[146:147] op_sel_hi:[1,0]
	v_pk_mul_f32 v[18:19], v[104:105], v[146:147] op_sel_hi:[1,0]
	v_pk_fma_f32 v[14:15], v[16:17], v[14:15], v[108:109]
	v_pk_fma_f32 v[12:13], v[12:13], v[18:19], v[96:97]
	v_min_f32_e32 v14, 0x40e00000, v14
	v_min_f32_e32 v15, 0x40e00000, v15
	v_pk_mul_f32 v[16:17], v[14:15], s[30:31] op_sel_hi:[1,0]
	v_med3_f32 v12, v12, s69, v193
	v_exp_f32_e32 v16, v16
	v_exp_f32_e32 v17, v17
	v_med3_f32 v13, v13, s69, v193
	v_pk_add_f32 v[12:13], v[12:13], 1.0 op_sel_hi:[1,0]
	v_cvt_f32_i32_e32 v7, v7
	v_pk_add_f32 v[16:17], v[16:17], 1.0 op_sel_hi:[1,0]
	v_cvt_f32_i32_e32 v6, v6
	v_rcp_f32_e32 v16, v16
	v_rcp_f32_e32 v17, v17
	v_max_f32_e64 v0, |v10|, |v11|
	v_cvt_f32_i32_e32 v3, v3
	v_cvt_f32_i32_e32 v2, v2
	v_pk_mul_f32 v[14:15], v[14:15], v[16:17]
	v_pk_mul_f32 v[16:17], v[74:75], v[146:147] op_sel_hi:[1,0]
	v_pk_mul_f32 v[12:13], v[12:13], v[14:15]
	v_pk_fma_f32 v[2:3], v[2:3], v[16:17], v[78:79]
	v_max_f32_e64 v14, |v12|, |v13|
	v_max3_f32 v0, v0, 0, v14
	v_pk_mul_f32 v[14:15], v[70:71], v[146:147] op_sel_hi:[1,0]
	v_cvt_f32_i32_e32 v9, v9
	v_pk_fma_f32 v[6:7], v[6:7], v[14:15], v[82:83]
	v_cvt_f32_i32_e32 v8, v8
	v_min_f32_e32 v6, 0x40e00000, v6
	v_min_f32_e32 v7, 0x40e00000, v7
	v_pk_mul_f32 v[14:15], v[6:7], s[30:31] op_sel_hi:[1,0]
	v_med3_f32 v2, v2, s69, v193
	v_exp_f32_e32 v14, v14
	v_exp_f32_e32 v15, v15
	v_med3_f32 v3, v3, s69, v193
	v_pk_add_f32 v[2:3], v[2:3], 1.0 op_sel_hi:[1,0]
	v_cvt_f32_i32_e32 v5, v5
	v_pk_add_f32 v[14:15], v[14:15], 1.0 op_sel_hi:[1,0]
	v_cvt_f32_i32_e32 v4, v4
	v_rcp_f32_e32 v14, v14
	v_rcp_f32_e32 v15, v15
	s_nop 0
	v_pk_mul_f32 v[6:7], v[6:7], v[14:15]
	s_nop 0
	v_pk_mul_f32 v[2:3], v[2:3], v[6:7]
	v_pk_mul_f32 v[6:7], v[72:73], v[146:147] op_sel_hi:[1,0]
	v_pk_mul_f32 v[14:15], v[76:77], v[146:147] op_sel_hi:[1,0]
	v_pk_fma_f32 v[6:7], v[8:9], v[6:7], v[84:85]
	v_pk_fma_f32 v[4:5], v[4:5], v[14:15], v[80:81]
	v_min_f32_e32 v6, 0x40e00000, v6
	v_min_f32_e32 v7, 0x40e00000, v7
	v_pk_mul_f32 v[8:9], v[6:7], s[30:31] op_sel_hi:[1,0]
	v_med3_f32 v4, v4, s69, v193
	v_exp_f32_e32 v8, v8
	v_exp_f32_e32 v9, v9
	v_med3_f32 v5, v5, s69, v193
	v_pk_add_f32 v[4:5], v[4:5], 1.0 op_sel_hi:[1,0]
	v_max_f32_e64 v16, |v2|, |v3|
	v_pk_add_f32 v[8:9], v[8:9], 1.0 op_sel_hi:[1,0]
	s_nop 0
	v_rcp_f32_e32 v8, v8
	v_rcp_f32_e32 v9, v9
	s_nop 0
	v_pk_mul_f32 v[6:7], v[6:7], v[8:9]
	s_nop 0
	v_pk_mul_f32 v[6:7], v[4:5], v[6:7]
	s_nop 0
	v_max_f32_e64 v4, |v6|, |v7|
	v_max3_f32 v0, v0, v16, v4
	v_mov_b32_e32 v5, v0
	s_nop 1
	v_permlane16_swap_b32_e32 v0, v5
	v_max_f32_e32 v0, v0, v5
	v_mov_b32_e32 v5, v0
	s_nop 1
	v_permlane32_swap_b32_e32 v0, v5
	v_add_u32_e32 v4, 0xb0, v178
	v_max_f32_e32 v8, v0, v5
	v_ashrrev_i32_e32 v5, 31, v4
	s_and_saveexec_b64 s[40:41], s[4:5]
	s_cbranch_execz .LBB0_1235
	s_lshl_b32 s42, s10, 2
	v_lshlrev_b64 v[14:15], 8, v[4:5]
	s_ashr_i32 s43, s42, 31
	v_lshl_add_u64 v[14:15], s[12:13], 0, v[14:15]
	v_lshl_add_u64 v[14:15], s[42:43], 2, v[14:15]
	s_lshl_b32 s16, s62, 2
	v_lshl_add_u64 v[14:15], v[14:15], 0, s[16:17]
	global_store_dword v[14:15], v8, off

.LBB0_1239:
	s_waitcnt vmcnt(0)
	s_barrier
	s_mov_b64 s[0:1], exec
	v_readlane_b32 s4, v252, 11
	v_readlane_b32 s5, v252, 12
	s_and_b64 s[4:5], s[0:1], s[4:5]
	s_mov_b64 exec, s[4:5]
	s_cbranch_execz .LBB0_1291
	s_add_i32 s4, 0, 0x26f20
	v_mov_b32_e32 v0, s4
	s_waitcnt vmcnt(0) expcnt(0) lgkmcnt(0)
	ds_read_b32 v3, v0
	s_add_i32 s4, 0, 0x26f24
	v_mov_b32_e32 v0, s4
	ds_read_b32 v1, v0
	s_waitcnt lgkmcnt(1)
	v_cmp_ne_u32_e32 vcc, 0, v3
	s_cbranch_vccnz .LBB0_1255
	v_readlane_b32 s4, v252, 4
	v_readlane_b32 s5, v252, 5
	s_load_dwordx2 s[10:11], s[4:5], 0x4
	v_readlane_b32 s42, v252, 2
	v_readlane_b32 s43, v252, 3
	s_add_u32 s4, s42, 0x4200
	s_addc_u32 s5, s43, 0
	s_add_u32 s6, s42, 0x4400
	s_addc_u32 s7, s43, 0
	v_readlane_b32 s14, v252, 6
	s_waitcnt lgkmcnt(0)
	s_mul_i32 s51, s10, s14
	s_add_u32 s10, s42, 0x4500
	s_mul_i32 s51, s51, s11
	s_addc_u32 s11, s43, 0
	v_readlane_b32 s15, v252, 7
	s_add_u32 s14, s42, 0x4600
	s_addc_u32 s15, s43, 0
	s_add_u32 s16, s42, 0x4700
	s_addc_u32 s17, s43, 0
	s_add_u32 s18, s42, 0x4800
	s_addc_u32 s19, s43, 0
	s_add_u32 s20, s42, 0x4900
	s_addc_u32 s21, s43, 0
	s_add_u32 s22, s42, 0x4a00
	s_addc_u32 s23, s43, 0
	s_add_u32 s24, s42, 0x4b00
	s_addc_u32 s25, s43, 0
	s_add_u32 s26, s42, 0x4c00
	s_addc_u32 s27, s43, 0
	s_add_u32 s28, s42, 0x4d00
	s_addc_u32 s29, s43, 0
	s_add_u32 s30, s42, 0x4e00
	s_addc_u32 s31, s43, 0
	s_add_u32 s34, s42, 0x4f00
	s_addc_u32 s35, s43, 0
	s_add_u32 s36, s42, 0x5000
	s_addc_u32 s37, s43, 0
	s_add_u32 s38, s42, 0x5100
	s_addc_u32 s39, s43, 0
	s_add_u32 s40, s42, 0x5200
	s_addc_u32 s41, s43, 0
	s_add_u32 s42, s42, 0x5300
	s_addc_u32 s43, s43, 0
	s_mov_b32 s52, 1
	v_mov_b32_e32 v17, 0
	s_branch .LBB0_1243
	s_nop 0
	s_nop 0
	s_nop 0
	s_nop 0
	s_nop 0
	s_nop 0
	s_nop 0
	s_nop 0
	s_nop 0
	s_nop 0
	s_nop 0
	s_nop 0
	s_nop 0
	s_nop 0
	s_nop 0
	s_nop 0
	s_nop 0
	s_nop 0
	s_nop 0
	s_nop 0
	s_nop 0
	s_nop 0
	s_nop 0
	s_nop 0
	s_nop 0
	s_nop 0
	s_nop 0
	s_nop 0
	s_nop 0
	s_nop 0
	s_nop 0
	s_nop 0

.LBB0_1370:
	v_readlane_b32 s64, v252, 13
	s_ashr_i32 s39, s38, 31
	v_readlane_b32 s74, v252, 23
	v_readlane_b32 s75, v252, 24
	v_lshl_or_b32 v176, s14, 8, v228
	s_lshl_b64 s[0:1], s[38:39], 13
	s_mov_b64 s[62:63], s[74:75]
	s_add_u32 s38, s62, s0
	v_ashrrev_i32_e32 v177, 31, v176
	v_lshl_add_u32 v200, s16, 8, v1
	s_addc_u32 s39, s63, s1
	v_lshlrev_b64 v[66:67], 2, v[176:177]
	v_or_b32_e32 v212, 32, v200
	v_lshl_add_u64 v[70:71], s[38:39], 0, v[66:67]
	v_readlane_b32 s38, v252, 50
	v_ashrrev_i32_e32 v201, 31, v200
	v_or_b32_e32 v218, 16, v200
	v_ashrrev_i32_e32 v213, 31, v212
	v_readlane_b32 s39, v252, 51
	s_add_u32 s0, s38, s0
	v_lshlrev_b64 v[82:83], 2, v[200:201]
	v_ashrrev_i32_e32 v219, 31, v218
	v_lshlrev_b64 v[180:181], 2, v[212:213]
	s_addc_u32 s1, s39, s1
	v_lshl_add_u64 v[84:85], s[20:21], 0, v[82:83]
	v_lshlrev_b64 v[96:97], 2, v[218:219]
	v_lshl_add_u64 v[182:183], s[20:21], 0, v[180:181]
	v_lshl_add_u64 v[94:95], s[0:1], 0, v[66:67]
	global_load_dwordx4 v[86:89], v[70:71], off offset:16
	global_load_dwordx4 v[98:101], v[70:71], off
	global_load_dwordx4 v[90:93], v[94:95], off offset:16
	global_load_dwordx4 v[102:105], v[94:95], off
	global_load_dwordx4 v[66:69], v[70:71], off offset:528
	s_nop 0
	global_load_dwordx4 v[70:73], v[70:71], off offset:512
	v_lshl_add_u64 v[82:83], s[10:11], 0, v[82:83]
	v_lshl_add_u64 v[178:179], s[20:21], 0, v[96:97]
	v_lshl_add_u64 v[96:97], s[10:11], 0, v[96:97]
	v_lshl_add_u64 v[180:181], s[10:11], 0, v[180:181]
	v_or_b32_e32 v206, 48, v200
	global_load_dword v220, v[84:85], off
	global_load_dword v222, v[82:83], off
	global_load_dword v214, v[178:179], off
	global_load_dword v216, v[96:97], off
	global_load_dword v208, v[182:183], off
	global_load_dword v210, v[180:181], off
	global_load_dword v198, v[82:83], off offset:512
	global_load_dword v196, v[84:85], off offset:512
	v_add_u32_e32 v194, 0x90, v200
	v_add_u32_e32 v188, 0xa0, v200
	v_add_u32_e32 v182, 0xb0, v200
	v_ashrrev_i32_e32 v207, 31, v206
	v_ashrrev_i32_e32 v195, 31, v194
	v_ashrrev_i32_e32 v189, 31, v188
	v_ashrrev_i32_e32 v183, 31, v182
	v_lshlrev_b64 v[184:185], 2, v[206:207]
	v_lshlrev_b64 v[82:83], 2, v[194:195]
	v_lshlrev_b64 v[96:97], 2, v[188:189]
	v_lshlrev_b64 v[180:181], 2, v[182:183]
	v_lshl_add_u64 v[186:187], s[20:21], 0, v[184:185]
	v_lshl_add_u64 v[184:185], s[10:11], 0, v[184:185]
	v_lshl_add_u64 v[84:85], s[20:21], 0, v[82:83]
	v_lshl_add_u64 v[82:83], s[10:11], 0, v[82:83]
	v_lshl_add_u64 v[178:179], s[20:21], 0, v[96:97]
	v_lshl_add_u64 v[96:97], s[10:11], 0, v[96:97]
	v_lshl_add_u64 v[224:225], s[20:21], 0, v[180:181]
	v_lshl_add_u64 v[180:181], s[10:11], 0, v[180:181]
	global_load_dword v202, v[186:187], off
	global_load_dword v204, v[184:185], off
	global_load_dword v190, v[84:85], off
	global_load_dword v192, v[82:83], off
	s_nop 0
	global_load_dword v184, v[178:179], off
	global_load_dword v186, v[96:97], off
	s_nop 0
	global_load_dword v178, v[224:225], off
	s_nop 0
	global_load_dword v180, v[180:181], off
	s_nop 0
	global_load_dwordx4 v[82:85], v[94:95], off offset:528
	s_nop 0
	global_load_dwordx4 v[94:97], v[94:95], off offset:512
	v_cvt_f32_i32_e32 v159, v159
	v_cvt_f32_i32_e32 v158, v158
	v_cvt_f32_i32_e32 v157, v157
	v_cvt_f32_i32_e32 v156, v156
	v_cvt_f32_i32_e32 v161, v161
	v_cvt_f32_i32_e32 v160, v160
	v_cvt_f32_i32_e32 v155, v155
	v_cvt_f32_i32_e32 v154, v154
	v_lshlrev_b64 v[232:233], 8, v[200:201]
	v_readlane_b32 s65, v252, 14
	v_readlane_b32 s66, v252, 15
	v_readlane_b32 s67, v252, 16
	v_readlane_b32 s68, v252, 17
	v_readlane_b32 s69, v252, 18
	v_readlane_b32 s70, v252, 19
	v_readlane_b32 s71, v252, 20
	v_readlane_b32 s72, v252, 21
	v_readlane_b32 s73, v252, 22
	v_readlane_b32 s76, v252, 25
	v_readlane_b32 s77, v252, 26
	v_readlane_b32 s78, v252, 27
	v_readlane_b32 s79, v252, 28
	s_waitcnt vmcnt(0)
	v_pk_mul_f32 v[238:239], v[92:93], v[222:223] op_sel_hi:[1,0]
	v_pk_mul_f32 v[224:225], v[102:103], v[222:223] op_sel_hi:[1,0]
	v_pk_mul_f32 v[234:235], v[104:105], v[222:223] op_sel_hi:[1,0]
	v_pk_mul_f32 v[236:237], v[90:91], v[222:223] op_sel_hi:[1,0]
	v_pk_fma_f32 v[158:159], v[158:159], v[224:225], v[98:99]
	v_pk_fma_f32 v[224:225], v[156:157], v[238:239], v[88:89]
	v_pk_fma_f32 v[160:161], v[160:161], v[234:235], v[100:101]
	v_pk_fma_f32 v[154:155], v[154:155], v[236:237], v[86:87]
	v_pk_mul_f32 v[224:225], v[220:221], v[224:225] op_sel_hi:[0,1]
	v_pk_mul_f32 v[156:157], v[220:221], v[158:159] op_sel_hi:[0,1]
	v_pk_mul_f32 v[158:159], v[220:221], v[160:161] op_sel_hi:[0,1]
	v_pk_mul_f32 v[160:161], v[220:221], v[154:155] op_sel_hi:[0,1]
	v_max_f32_e64 v155, |v224|, |v225|
	v_max_f32_e64 v0, |v156|, |v157|
	v_max_f32_e64 v154, |v158|, |v159|
	v_max3_f32 v155, |v160|, |v161|, v155
	v_max3_f32 v0, v0, v154, v155
	v_mov_b32_e32 v154, v0
	s_nop 1
	v_permlane16_swap_b32_e32 v0, v154
	v_max_f32_e32 v0, v0, v154
	v_mov_b32_e32 v154, v0
	s_nop 1
	v_permlane32_swap_b32_e32 v0, v154
	v_max_f32_e32 v179, v0, v154
	v_lshl_add_u64 v[154:155], s[12:13], 0, v[232:233]
	s_and_saveexec_b64 s[0:1], s[4:5]
	s_cbranch_execz .LBB0_1372
	s_lshl_b32 s38, s14, 3
	s_ashr_i32 s39, s38, 31
	v_lshl_add_u64 v[232:233], s[38:39], 2, v[154:155]
	s_lshl_b32 s16, s52, 2
	v_lshl_add_u64 v[232:233], v[232:233], 0, s[16:17]
	v_mul_f32_e32 v0, 0x3c010204, v179
	global_store_dword v[232:233], v0, off
.LBB0_1372:
	s_or_b64 exec, exec, s[0:1]
	v_rcp_f32_e32 v0, v179
	v_cmp_lt_f32_e32 vcc, 0, v179
	v_lshlrev_b64 v[232:233], 11, v[200:201]
	v_cvt_f32_i32_e32 v151, v151
	v_mul_f32_e32 v0, 0x42fe0000, v0
	v_cndmask_b32_e32 v0, 0, v0, vcc
	v_pk_mul_f32 v[156:157], v[156:157], v[0:1] op_sel_hi:[1,0]
	v_pk_mul_f32 v[158:159], v[158:159], v[0:1] op_sel_hi:[1,0]
	v_pk_mul_f32 v[160:161], v[160:161], v[0:1] op_sel_hi:[1,0]
	v_pk_mul_f32 v[224:225], v[224:225], v[0:1] op_sel_hi:[1,0]
	v_add_f32_e32 v0, 0x4b400000, v156
	v_add_f32_e32 v156, 0x4b400000, v157
	v_add_f32_e32 v157, 0x4b400000, v158
	v_add_f32_e32 v158, 0x4b400000, v159
	v_perm_b32 v0, v156, v0, s59
	v_perm_b32 v156, v158, v157, s59
	v_lshl_or_b32 v158, v156, 16, v0
	v_add_f32_e32 v0, 0x4b400000, v160
	v_add_f32_e32 v156, 0x4b400000, v161
	v_add_f32_e32 v157, 0x4b400000, v224
	v_add_f32_e32 v159, 0x4b400000, v225
	v_perm_b32 v0, v156, v0, s59
	v_perm_b32 v156, v159, v157, s59
	v_cvt_f32_i32_e32 v150, v150
	v_lshl_or_b32 v159, v156, 16, v0
	v_lshl_add_u64 v[156:157], s[8:9], 0, v[232:233]
	v_cvt_f32_i32_e32 v153, v153
	v_cvt_f32_i32_e32 v152, v152
	v_mov_b32_e32 v223, v222
	v_lshl_add_u64 v[156:157], v[156:157], 0, v[176:177]
	v_cvt_f32_i32_e32 v147, v147
	v_cvt_f32_i32_e32 v146, v146
	global_store_dwordx2 v[156:157], v[158:159], off
	v_pk_mul_f32 v[158:159], v[94:95], v[222:223]
	v_cvt_f32_i32_e32 v149, v149
	v_cvt_f32_i32_e32 v148, v148
	v_pk_fma_f32 v[150:151], v[150:151], v[158:159], v[70:71]
	v_pk_mul_f32 v[158:159], v[96:97], v[222:223]
	v_mov_b32_e32 v221, v220
	v_pk_fma_f32 v[152:153], v[152:153], v[158:159], v[72:73]
	v_pk_mul_f32 v[158:159], v[82:83], v[222:223]
	v_pk_mul_f32 v[150:151], v[220:221], v[150:151]
	v_pk_fma_f32 v[146:147], v[146:147], v[158:159], v[66:67]
	v_pk_mul_f32 v[158:159], v[84:85], v[222:223]
	v_pk_mul_f32 v[152:153], v[220:221], v[152:153]
	v_pk_fma_f32 v[148:149], v[148:149], v[158:159], v[68:69]
	v_pk_mul_f32 v[146:147], v[220:221], v[146:147]
	v_pk_mul_f32 v[148:149], v[220:221], v[148:149]
	v_max_f32_e64 v0, |v150|, |v151|
	v_max_f32_e64 v159, |v148|, |v149|
	v_max_f32_e64 v158, |v152|, |v153|
	v_max3_f32 v159, |v146|, |v147|, v159
	v_max3_f32 v0, v0, v158, v159
	v_mov_b32_e32 v158, v0
	s_nop 1
	v_permlane16_swap_b32_e32 v0, v158
	v_max_f32_e32 v0, v0, v158
	v_mov_b32_e32 v158, v0
	s_nop 1
	v_permlane32_swap_b32_e32 v0, v158
	v_max_f32_e32 v158, v0, v158
	s_and_saveexec_b64 s[0:1], s[4:5]
	s_cbranch_execz .LBB0_1374
	s_lshl_b32 s38, s14, 3
	s_ashr_i32 s39, s38, 31
	v_lshl_add_u64 v[154:155], s[38:39], 2, v[154:155]
	s_lshl_b32 s16, s52, 2
	v_lshl_add_u64 v[154:155], v[154:155], 0, s[16:17]
	v_mul_f32_e32 v0, 0x3c010204, v158
	global_store_dword v[154:155], v0, off offset:16
.LBB0_1374:
	s_or_b64 exec, exec, s[0:1]
	v_rcp_f32_e32 v0, v158
	v_cmp_lt_f32_e32 vcc, 0, v158
	v_cvt_f32_i32_e32 v143, v143
	v_cvt_f32_i32_e32 v142, v142
	v_mul_f32_e32 v0, 0x42fe0000, v0
	v_cndmask_b32_e32 v0, 0, v0, vcc
	v_pk_mul_f32 v[150:151], v[150:151], v[0:1] op_sel_hi:[1,0]
	v_pk_mul_f32 v[152:153], v[152:153], v[0:1] op_sel_hi:[1,0]
	v_pk_mul_f32 v[146:147], v[146:147], v[0:1] op_sel_hi:[1,0]
	v_pk_mul_f32 v[148:149], v[148:149], v[0:1] op_sel_hi:[1,0]
	v_add_f32_e32 v0, 0x4b400000, v150
	v_add_f32_e32 v150, 0x4b400000, v151
	v_add_f32_e32 v151, 0x4b400000, v152
	v_add_f32_e32 v152, 0x4b400000, v153
	v_perm_b32 v0, v150, v0, s59
	v_perm_b32 v150, v152, v151, s59
	v_lshl_or_b32 v150, v150, 16, v0
	v_add_f32_e32 v0, 0x4b400000, v146
	v_add_f32_e32 v146, 0x4b400000, v147
	v_add_f32_e32 v147, 0x4b400000, v148
	v_add_f32_e32 v148, 0x4b400000, v149
	v_cvt_f32_i32_e32 v145, v145
	v_cvt_f32_i32_e32 v144, v144
	v_perm_b32 v0, v146, v0, s59
	v_perm_b32 v146, v148, v147, s59
	v_cvt_f32_i32_e32 v139, v139
	v_cvt_f32_i32_e32 v138, v138
	v_lshl_or_b32 v151, v146, 16, v0
	v_pk_mul_f32 v[146:147], v[102:103], v[216:217] op_sel_hi:[1,0]
	v_cvt_f32_i32_e32 v149, v141
	v_pk_fma_f32 v[142:143], v[142:143], v[146:147], v[98:99]
	v_pk_mul_f32 v[146:147], v[104:105], v[216:217] op_sel_hi:[1,0]
	v_cvt_f32_i32_e32 v148, v140
	v_pk_fma_f32 v[144:145], v[144:145], v[146:147], v[100:101]
	v_pk_mul_f32 v[146:147], v[90:91], v[216:217] op_sel_hi:[1,0]
	v_pk_mul_f32 v[142:143], v[214:215], v[142:143] op_sel_hi:[0,1]
	v_pk_fma_f32 v[138:139], v[138:139], v[146:147], v[86:87]
	v_pk_mul_f32 v[144:145], v[214:215], v[144:145] op_sel_hi:[0,1]
	v_pk_mul_f32 v[140:141], v[214:215], v[138:139] op_sel_hi:[0,1]
	v_pk_mul_f32 v[138:139], v[92:93], v[216:217] op_sel_hi:[1,0]
	v_max_f32_e64 v0, |v142|, |v143|
	v_pk_fma_f32 v[138:139], v[148:149], v[138:139], v[88:89]
	global_store_dwordx2 v[156:157], v[150:151], off offset:128
	v_pk_mul_f32 v[146:147], v[214:215], v[138:139] op_sel_hi:[0,1]
	v_max_f32_e64 v139, |v146|, |v147|
	v_max_f32_e64 v138, |v144|, |v145|
	v_max3_f32 v139, |v140|, |v141|, v139
	v_max3_f32 v0, v0, v138, v139
	v_mov_b32_e32 v138, v0
	s_nop 1
	v_permlane16_swap_b32_e32 v0, v138
	v_max_f32_e32 v0, v0, v138
	v_mov_b32_e32 v138, v0
	s_nop 1
	v_permlane32_swap_b32_e32 v0, v138
	v_lshlrev_b64 v[150:151], 8, v[218:219]
	v_max_f32_e32 v148, v0, v138
	v_lshl_add_u64 v[138:139], s[12:13], 0, v[150:151]
	s_and_saveexec_b64 s[0:1], s[4:5]
	s_cbranch_execz .LBB0_1376
	s_lshl_b32 s38, s14, 3
	s_ashr_i32 s39, s38, 31
	v_lshl_add_u64 v[150:151], s[38:39], 2, v[138:139]
	s_lshl_b32 s16, s52, 2
	v_lshl_add_u64 v[150:151], v[150:151], 0, s[16:17]
	v_mul_f32_e32 v0, 0x3c010204, v148
	global_store_dword v[150:151], v0, off
.LBB0_1376:
	s_or_b64 exec, exec, s[0:1]
	v_rcp_f32_e32 v0, v148
	v_cmp_lt_f32_e32 vcc, 0, v148
	v_lshlrev_b64 v[150:151], 11, v[218:219]
	v_cvt_f32_i32_e32 v135, v135
	v_mul_f32_e32 v0, 0x42fe0000, v0
	v_cndmask_b32_e32 v0, 0, v0, vcc
	v_pk_mul_f32 v[142:143], v[142:143], v[0:1] op_sel_hi:[1,0]
	v_pk_mul_f32 v[144:145], v[144:145], v[0:1] op_sel_hi:[1,0]
	v_pk_mul_f32 v[140:141], v[140:141], v[0:1] op_sel_hi:[1,0]
	v_pk_mul_f32 v[146:147], v[146:147], v[0:1] op_sel_hi:[1,0]
	v_add_f32_e32 v0, 0x4b400000, v142
	v_add_f32_e32 v142, 0x4b400000, v143
	v_add_f32_e32 v143, 0x4b400000, v144
	v_add_f32_e32 v144, 0x4b400000, v145
	v_perm_b32 v0, v142, v0, s59
	v_perm_b32 v142, v144, v143, s59
	v_lshl_or_b32 v142, v142, 16, v0
	v_add_f32_e32 v0, 0x4b400000, v140
	v_add_f32_e32 v140, 0x4b400000, v141
	v_add_f32_e32 v141, 0x4b400000, v146
	v_add_f32_e32 v143, 0x4b400000, v147
	v_perm_b32 v0, v140, v0, s59
	v_perm_b32 v140, v143, v141, s59
	v_cvt_f32_i32_e32 v134, v134
	v_lshl_or_b32 v143, v140, 16, v0
	v_lshl_add_u64 v[140:141], s[8:9], 0, v[150:151]
	v_cvt_f32_i32_e32 v137, v137
	v_cvt_f32_i32_e32 v136, v136
	v_mov_b32_e32 v217, v216
	v_lshl_add_u64 v[140:141], v[140:141], 0, v[176:177]
	v_cvt_f32_i32_e32 v131, v131
	v_cvt_f32_i32_e32 v130, v130
	global_store_dwordx2 v[140:141], v[142:143], off
	v_pk_mul_f32 v[142:143], v[94:95], v[216:217]
	v_cvt_f32_i32_e32 v133, v133
	v_cvt_f32_i32_e32 v132, v132
	v_pk_fma_f32 v[134:135], v[134:135], v[142:143], v[70:71]
	v_pk_mul_f32 v[142:143], v[96:97], v[216:217]
	v_mov_b32_e32 v215, v214
	v_pk_fma_f32 v[136:137], v[136:137], v[142:143], v[72:73]
	v_pk_mul_f32 v[142:143], v[82:83], v[216:217]
	v_pk_mul_f32 v[134:135], v[214:215], v[134:135]
	v_pk_fma_f32 v[130:131], v[130:131], v[142:143], v[66:67]
	v_pk_mul_f32 v[142:143], v[84:85], v[216:217]
	v_pk_mul_f32 v[136:137], v[214:215], v[136:137]
	v_pk_fma_f32 v[132:133], v[132:133], v[142:143], v[68:69]
	v_pk_mul_f32 v[130:131], v[214:215], v[130:131]
	v_pk_mul_f32 v[132:133], v[214:215], v[132:133]
	v_max_f32_e64 v0, |v134|, |v135|
	v_max_f32_e64 v143, |v132|, |v133|
	v_max_f32_e64 v142, |v136|, |v137|
	v_max3_f32 v143, |v130|, |v131|, v143
	v_max3_f32 v0, v0, v142, v143
	v_mov_b32_e32 v142, v0
	s_nop 1
	v_permlane16_swap_b32_e32 v0, v142
	v_max_f32_e32 v0, v0, v142
	v_mov_b32_e32 v142, v0
	s_nop 1
	v_permlane32_swap_b32_e32 v0, v142
	v_max_f32_e32 v142, v0, v142
	s_and_saveexec_b64 s[0:1], s[4:5]
	s_cbranch_execz .LBB0_1378
	s_lshl_b32 s38, s14, 3
	s_ashr_i32 s39, s38, 31
	v_lshl_add_u64 v[138:139], s[38:39], 2, v[138:139]
	s_lshl_b32 s16, s52, 2
	v_lshl_add_u64 v[138:139], v[138:139], 0, s[16:17]
	v_mul_f32_e32 v0, 0x3c010204, v142
	global_store_dword v[138:139], v0, off offset:16
.LBB0_1378:
	s_or_b64 exec, exec, s[0:1]
	v_rcp_f32_e32 v0, v142
	v_cmp_lt_f32_e32 vcc, 0, v142
	v_cvt_f32_i32_e32 v127, v127
	v_cvt_f32_i32_e32 v126, v126
	v_mul_f32_e32 v0, 0x42fe0000, v0
	v_cndmask_b32_e32 v0, 0, v0, vcc
	v_pk_mul_f32 v[134:135], v[134:135], v[0:1] op_sel_hi:[1,0]
	v_pk_mul_f32 v[136:137], v[136:137], v[0:1] op_sel_hi:[1,0]
	v_pk_mul_f32 v[130:131], v[130:131], v[0:1] op_sel_hi:[1,0]
	v_pk_mul_f32 v[132:133], v[132:133], v[0:1] op_sel_hi:[1,0]
	v_add_f32_e32 v0, 0x4b400000, v134
	v_add_f32_e32 v134, 0x4b400000, v135
	v_add_f32_e32 v135, 0x4b400000, v136
	v_add_f32_e32 v136, 0x4b400000, v137
	v_perm_b32 v0, v134, v0, s59
	v_perm_b32 v134, v136, v135, s59
	v_lshl_or_b32 v134, v134, 16, v0
	v_add_f32_e32 v0, 0x4b400000, v130
	v_add_f32_e32 v130, 0x4b400000, v131
	v_add_f32_e32 v131, 0x4b400000, v132
	v_add_f32_e32 v132, 0x4b400000, v133
	v_cvt_f32_i32_e32 v129, v129
	v_cvt_f32_i32_e32 v128, v128
	v_perm_b32 v0, v130, v0, s59
	v_perm_b32 v130, v132, v131, s59
	v_cvt_f32_i32_e32 v123, v123
	v_cvt_f32_i32_e32 v122, v122
	v_lshl_or_b32 v135, v130, 16, v0
	v_pk_mul_f32 v[130:131], v[102:103], v[210:211] op_sel_hi:[1,0]
	v_cvt_f32_i32_e32 v133, v125
	v_pk_fma_f32 v[126:127], v[126:127], v[130:131], v[98:99]
	v_pk_mul_f32 v[130:131], v[104:105], v[210:211] op_sel_hi:[1,0]
	v_cvt_f32_i32_e32 v132, v124
	v_pk_fma_f32 v[128:129], v[128:129], v[130:131], v[100:101]
	v_pk_mul_f32 v[130:131], v[90:91], v[210:211] op_sel_hi:[1,0]
	v_pk_mul_f32 v[126:127], v[208:209], v[126:127] op_sel_hi:[0,1]
	v_pk_fma_f32 v[122:123], v[122:123], v[130:131], v[86:87]
	v_pk_mul_f32 v[128:129], v[208:209], v[128:129] op_sel_hi:[0,1]
	v_pk_mul_f32 v[124:125], v[208:209], v[122:123] op_sel_hi:[0,1]
	v_pk_mul_f32 v[122:123], v[92:93], v[210:211] op_sel_hi:[1,0]
	v_max_f32_e64 v0, |v126|, |v127|
	v_pk_fma_f32 v[122:123], v[132:133], v[122:123], v[88:89]
	global_store_dwordx2 v[140:141], v[134:135], off offset:128
	v_pk_mul_f32 v[130:131], v[208:209], v[122:123] op_sel_hi:[0,1]
	v_max_f32_e64 v123, |v130|, |v131|
	v_max_f32_e64 v122, |v128|, |v129|
	v_max3_f32 v123, |v124|, |v125|, v123
	v_max3_f32 v0, v0, v122, v123
	v_mov_b32_e32 v122, v0
	s_nop 1
	v_permlane16_swap_b32_e32 v0, v122
	v_max_f32_e32 v0, v0, v122
	v_mov_b32_e32 v122, v0
	s_nop 1
	v_permlane32_swap_b32_e32 v0, v122
	v_lshlrev_b64 v[134:135], 8, v[212:213]
	v_max_f32_e32 v132, v0, v122
	v_lshl_add_u64 v[122:123], s[12:13], 0, v[134:135]
	s_and_saveexec_b64 s[0:1], s[4:5]
	s_cbranch_execz .LBB0_1380
	s_lshl_b32 s38, s14, 3
	s_ashr_i32 s39, s38, 31
	v_lshl_add_u64 v[134:135], s[38:39], 2, v[122:123]
	s_lshl_b32 s16, s52, 2
	v_lshl_add_u64 v[134:135], v[134:135], 0, s[16:17]
	v_mul_f32_e32 v0, 0x3c010204, v132
	global_store_dword v[134:135], v0, off
.LBB0_1380:
	s_or_b64 exec, exec, s[0:1]
	v_rcp_f32_e32 v0, v132
	v_cmp_lt_f32_e32 vcc, 0, v132
	v_lshlrev_b64 v[134:135], 11, v[212:213]
	v_cvt_f32_i32_e32 v119, v119
	v_mul_f32_e32 v0, 0x42fe0000, v0
	v_cndmask_b32_e32 v0, 0, v0, vcc
	v_pk_mul_f32 v[126:127], v[126:127], v[0:1] op_sel_hi:[1,0]
	v_pk_mul_f32 v[128:129], v[128:129], v[0:1] op_sel_hi:[1,0]
	v_pk_mul_f32 v[124:125], v[124:125], v[0:1] op_sel_hi:[1,0]
	v_pk_mul_f32 v[130:131], v[130:131], v[0:1] op_sel_hi:[1,0]
	v_add_f32_e32 v0, 0x4b400000, v126
	v_add_f32_e32 v126, 0x4b400000, v127
	v_add_f32_e32 v127, 0x4b400000, v128
	v_add_f32_e32 v128, 0x4b400000, v129
	v_perm_b32 v0, v126, v0, s59
	v_perm_b32 v126, v128, v127, s59
	v_lshl_or_b32 v126, v126, 16, v0
	v_add_f32_e32 v0, 0x4b400000, v124
	v_add_f32_e32 v124, 0x4b400000, v125
	v_add_f32_e32 v125, 0x4b400000, v130
	v_add_f32_e32 v127, 0x4b400000, v131
	v_perm_b32 v0, v124, v0, s59
	v_perm_b32 v124, v127, v125, s59
	v_cvt_f32_i32_e32 v118, v118
	v_lshl_or_b32 v127, v124, 16, v0
	v_lshl_add_u64 v[124:125], s[8:9], 0, v[134:135]
	v_cvt_f32_i32_e32 v121, v121
	v_cvt_f32_i32_e32 v120, v120
	v_mov_b32_e32 v211, v210
	v_lshl_add_u64 v[124:125], v[124:125], 0, v[176:177]
	v_cvt_f32_i32_e32 v115, v115
	v_cvt_f32_i32_e32 v114, v114
	global_store_dwordx2 v[124:125], v[126:127], off
	v_pk_mul_f32 v[126:127], v[94:95], v[210:211]
	v_cvt_f32_i32_e32 v117, v117
	v_cvt_f32_i32_e32 v116, v116
	v_pk_fma_f32 v[118:119], v[118:119], v[126:127], v[70:71]
	v_pk_mul_f32 v[126:127], v[96:97], v[210:211]
	v_mov_b32_e32 v209, v208
	v_pk_fma_f32 v[120:121], v[120:121], v[126:127], v[72:73]
	v_pk_mul_f32 v[126:127], v[82:83], v[210:211]
	v_pk_mul_f32 v[118:119], v[208:209], v[118:119]
	v_pk_fma_f32 v[114:115], v[114:115], v[126:127], v[66:67]
	v_pk_mul_f32 v[126:127], v[84:85], v[210:211]
	v_pk_mul_f32 v[120:121], v[208:209], v[120:121]
	v_pk_fma_f32 v[116:117], v[116:117], v[126:127], v[68:69]
	v_pk_mul_f32 v[114:115], v[208:209], v[114:115]
	v_pk_mul_f32 v[116:117], v[208:209], v[116:117]
	v_max_f32_e64 v0, |v118|, |v119|
	v_max_f32_e64 v127, |v116|, |v117|
	v_max_f32_e64 v126, |v120|, |v121|
	v_max3_f32 v127, |v114|, |v115|, v127
	v_max3_f32 v0, v0, v126, v127
	v_mov_b32_e32 v126, v0
	s_nop 1
	v_permlane16_swap_b32_e32 v0, v126
	v_max_f32_e32 v0, v0, v126
	v_mov_b32_e32 v126, v0
	s_nop 1
	v_permlane32_swap_b32_e32 v0, v126
	v_max_f32_e32 v126, v0, v126
	s_and_saveexec_b64 s[0:1], s[4:5]
	s_cbranch_execz .LBB0_1382
	s_lshl_b32 s38, s14, 3
	s_ashr_i32 s39, s38, 31
	v_lshl_add_u64 v[122:123], s[38:39], 2, v[122:123]
	s_lshl_b32 s16, s52, 2
	v_lshl_add_u64 v[122:123], v[122:123], 0, s[16:17]
	v_mul_f32_e32 v0, 0x3c010204, v126
	global_store_dword v[122:123], v0, off offset:16
.LBB0_1382:
	s_or_b64 exec, exec, s[0:1]
	v_rcp_f32_e32 v0, v126
	v_cmp_lt_f32_e32 vcc, 0, v126
	v_cvt_f32_i32_e32 v111, v111
	v_cvt_f32_i32_e32 v110, v110
	v_mul_f32_e32 v0, 0x42fe0000, v0
	v_cndmask_b32_e32 v0, 0, v0, vcc
	v_pk_mul_f32 v[118:119], v[118:119], v[0:1] op_sel_hi:[1,0]
	v_pk_mul_f32 v[120:121], v[120:121], v[0:1] op_sel_hi:[1,0]
	v_pk_mul_f32 v[114:115], v[114:115], v[0:1] op_sel_hi:[1,0]
	v_pk_mul_f32 v[116:117], v[116:117], v[0:1] op_sel_hi:[1,0]
	v_add_f32_e32 v0, 0x4b400000, v118
	v_add_f32_e32 v118, 0x4b400000, v119
	v_add_f32_e32 v119, 0x4b400000, v120
	v_add_f32_e32 v120, 0x4b400000, v121
	v_perm_b32 v0, v118, v0, s59
	v_perm_b32 v118, v120, v119, s59
	v_lshl_or_b32 v118, v118, 16, v0
	v_add_f32_e32 v0, 0x4b400000, v114
	v_add_f32_e32 v114, 0x4b400000, v115
	v_add_f32_e32 v115, 0x4b400000, v116
	v_add_f32_e32 v116, 0x4b400000, v117
	v_cvt_f32_i32_e32 v113, v113
	v_cvt_f32_i32_e32 v112, v112
	v_perm_b32 v0, v114, v0, s59
	v_perm_b32 v114, v116, v115, s59
	v_cvt_f32_i32_e32 v107, v107
	v_cvt_f32_i32_e32 v106, v106
	v_lshl_or_b32 v119, v114, 16, v0
	v_pk_mul_f32 v[114:115], v[102:103], v[204:205] op_sel_hi:[1,0]
	v_cvt_f32_i32_e32 v117, v109
	v_pk_fma_f32 v[110:111], v[110:111], v[114:115], v[98:99]
	v_pk_mul_f32 v[114:115], v[104:105], v[204:205] op_sel_hi:[1,0]
	v_cvt_f32_i32_e32 v116, v108
	v_pk_fma_f32 v[112:113], v[112:113], v[114:115], v[100:101]
	v_pk_mul_f32 v[114:115], v[90:91], v[204:205] op_sel_hi:[1,0]
	v_pk_mul_f32 v[110:111], v[202:203], v[110:111] op_sel_hi:[0,1]
	v_pk_fma_f32 v[106:107], v[106:107], v[114:115], v[86:87]
	v_pk_mul_f32 v[112:113], v[202:203], v[112:113] op_sel_hi:[0,1]
	v_pk_mul_f32 v[108:109], v[202:203], v[106:107] op_sel_hi:[0,1]
	v_pk_mul_f32 v[106:107], v[92:93], v[204:205] op_sel_hi:[1,0]
	v_max_f32_e64 v0, |v110|, |v111|
	v_pk_fma_f32 v[106:107], v[116:117], v[106:107], v[88:89]
	global_store_dwordx2 v[124:125], v[118:119], off offset:128
	v_pk_mul_f32 v[114:115], v[202:203], v[106:107] op_sel_hi:[0,1]
	v_max_f32_e64 v107, |v114|, |v115|
	v_max_f32_e64 v106, |v112|, |v113|
	v_max3_f32 v107, |v108|, |v109|, v107
	v_max3_f32 v0, v0, v106, v107
	v_mov_b32_e32 v106, v0
	s_nop 1
	v_permlane16_swap_b32_e32 v0, v106
	v_max_f32_e32 v0, v0, v106
	v_mov_b32_e32 v106, v0
	s_nop 1
	v_permlane32_swap_b32_e32 v0, v106
	v_lshlrev_b64 v[118:119], 8, v[206:207]
	v_max_f32_e32 v116, v0, v106
	v_lshl_add_u64 v[106:107], s[12:13], 0, v[118:119]
	s_and_saveexec_b64 s[0:1], s[4:5]
	s_cbranch_execz .LBB0_1384
	s_lshl_b32 s38, s14, 3
	s_ashr_i32 s39, s38, 31
	v_lshl_add_u64 v[118:119], s[38:39], 2, v[106:107]
	s_lshl_b32 s16, s52, 2
	v_lshl_add_u64 v[118:119], v[118:119], 0, s[16:17]
	v_mul_f32_e32 v0, 0x3c010204, v116
	global_store_dword v[118:119], v0, off
.LBB0_1384:
	s_or_b64 exec, exec, s[0:1]
	v_rcp_f32_e32 v0, v116
	v_cmp_lt_f32_e32 vcc, 0, v116
	v_lshlrev_b64 v[118:119], 11, v[206:207]
	v_cvt_f32_i32_e32 v79, v79
	v_mul_f32_e32 v0, 0x42fe0000, v0
	v_cndmask_b32_e32 v0, 0, v0, vcc
	v_pk_mul_f32 v[110:111], v[110:111], v[0:1] op_sel_hi:[1,0]
	v_pk_mul_f32 v[112:113], v[112:113], v[0:1] op_sel_hi:[1,0]
	v_pk_mul_f32 v[108:109], v[108:109], v[0:1] op_sel_hi:[1,0]
	v_pk_mul_f32 v[114:115], v[114:115], v[0:1] op_sel_hi:[1,0]
	v_add_f32_e32 v0, 0x4b400000, v110
	v_add_f32_e32 v110, 0x4b400000, v111
	v_add_f32_e32 v111, 0x4b400000, v112
	v_add_f32_e32 v112, 0x4b400000, v113
	v_perm_b32 v0, v110, v0, s59
	v_perm_b32 v110, v112, v111, s59
	v_lshl_or_b32 v110, v110, 16, v0
	v_add_f32_e32 v0, 0x4b400000, v108
	v_add_f32_e32 v108, 0x4b400000, v109
	v_add_f32_e32 v109, 0x4b400000, v114
	v_add_f32_e32 v111, 0x4b400000, v115
	v_perm_b32 v0, v108, v0, s59
	v_perm_b32 v108, v111, v109, s59
	v_cvt_f32_i32_e32 v78, v78
	v_lshl_or_b32 v111, v108, 16, v0
	v_lshl_add_u64 v[108:109], s[8:9], 0, v[118:119]
	v_cvt_f32_i32_e32 v81, v81
	v_cvt_f32_i32_e32 v80, v80
	v_mov_b32_e32 v205, v204
	v_lshl_add_u64 v[108:109], v[108:109], 0, v[176:177]
	v_cvt_f32_i32_e32 v75, v75
	v_cvt_f32_i32_e32 v74, v74
	global_store_dwordx2 v[108:109], v[110:111], off
	v_pk_mul_f32 v[110:111], v[94:95], v[204:205]
	v_cvt_f32_i32_e32 v113, v77
	v_pk_fma_f32 v[78:79], v[78:79], v[110:111], v[70:71]
	v_pk_mul_f32 v[110:111], v[96:97], v[204:205]
	v_cvt_f32_i32_e32 v112, v76
	v_pk_fma_f32 v[80:81], v[80:81], v[110:111], v[72:73]
	v_pk_mul_f32 v[110:111], v[82:83], v[204:205]
	v_mov_b32_e32 v203, v202
	v_pk_fma_f32 v[74:75], v[74:75], v[110:111], v[66:67]
	v_pk_mul_f32 v[78:79], v[202:203], v[78:79]
	v_pk_mul_f32 v[76:77], v[202:203], v[74:75]
	v_pk_mul_f32 v[74:75], v[84:85], v[204:205]
	v_pk_mul_f32 v[80:81], v[202:203], v[80:81]
	v_pk_fma_f32 v[74:75], v[112:113], v[74:75], v[68:69]
	v_max_f32_e64 v0, |v78|, |v79|
	v_pk_mul_f32 v[110:111], v[202:203], v[74:75]
	v_max_f32_e64 v74, |v80|, |v81|
	v_max_f32_e64 v75, |v110|, |v111|
	v_max3_f32 v75, |v76|, |v77|, v75
	v_max3_f32 v0, v0, v74, v75
	v_mov_b32_e32 v74, v0
	s_nop 1
	v_permlane16_swap_b32_e32 v0, v74
	v_max_f32_e32 v0, v0, v74
	v_mov_b32_e32 v74, v0
	s_nop 1
	v_permlane32_swap_b32_e32 v0, v74
	v_max_f32_e32 v112, v0, v74
	s_and_saveexec_b64 s[0:1], s[4:5]
	s_cbranch_execz .LBB0_1386
	s_lshl_b32 s38, s14, 3
	s_ashr_i32 s39, s38, 31
	v_lshl_add_u64 v[74:75], s[38:39], 2, v[106:107]
	s_lshl_b32 s16, s52, 2
	v_lshl_add_u64 v[74:75], v[74:75], 0, s[16:17]
	v_mul_f32_e32 v0, 0x3c010204, v112
	global_store_dword v[74:75], v0, off offset:16
.LBB0_1386:
	s_or_b64 exec, exec, s[0:1]
	v_rcp_f32_e32 v0, v112
	v_cmp_lt_f32_e32 vcc, 0, v112
	v_cvt_f32_i32_e32 v63, v63
	v_cvt_f32_i32_e32 v62, v62
	v_mul_f32_e32 v0, 0x42fe0000, v0
	v_cndmask_b32_e32 v0, 0, v0, vcc
	v_pk_mul_f32 v[78:79], v[78:79], v[0:1] op_sel_hi:[1,0]
	v_pk_mul_f32 v[80:81], v[80:81], v[0:1] op_sel_hi:[1,0]
	v_pk_mul_f32 v[76:77], v[76:77], v[0:1] op_sel_hi:[1,0]
	v_pk_mul_f32 v[106:107], v[110:111], v[0:1] op_sel_hi:[1,0]
	v_add_f32_e32 v0, 0x4b400000, v78
	v_add_f32_e32 v78, 0x4b400000, v79
	v_add_f32_e32 v79, 0x4b400000, v80
	v_add_f32_e32 v80, 0x4b400000, v81
	v_perm_b32 v0, v78, v0, s59
	v_perm_b32 v78, v80, v79, s59
	v_lshl_or_b32 v78, v78, 16, v0
	v_add_f32_e32 v0, 0x4b400000, v76
	v_add_f32_e32 v76, 0x4b400000, v77
	v_add_f32_e32 v77, 0x4b400000, v106
	v_add_f32_e32 v79, 0x4b400000, v107
	v_cvt_f32_i32_e32 v65, v65
	v_cvt_f32_i32_e32 v64, v64
	v_perm_b32 v0, v76, v0, s59
	v_perm_b32 v76, v79, v77, s59
	v_cvt_f32_i32_e32 v59, v59
	v_cvt_f32_i32_e32 v58, v58
	v_lshl_or_b32 v79, v76, 16, v0
	v_pk_mul_f32 v[76:77], v[102:103], v[198:199] op_sel_hi:[1,0]
	global_store_dwordx2 v[108:109], v[78:79], off offset:128
	v_pk_fma_f32 v[62:63], v[62:63], v[76:77], v[98:99]
	v_pk_mul_f32 v[76:77], v[104:105], v[198:199] op_sel_hi:[1,0]
	v_cvt_f32_i32_e32 v79, v61
	v_cvt_f32_i32_e32 v78, v60
	v_pk_fma_f32 v[64:65], v[64:65], v[76:77], v[100:101]
	v_pk_mul_f32 v[76:77], v[90:91], v[198:199] op_sel_hi:[1,0]
	v_pk_mul_f32 v[62:63], v[196:197], v[62:63] op_sel_hi:[0,1]
	v_pk_fma_f32 v[58:59], v[58:59], v[76:77], v[86:87]
	v_pk_mul_f32 v[64:65], v[196:197], v[64:65] op_sel_hi:[0,1]
	v_pk_mul_f32 v[60:61], v[196:197], v[58:59] op_sel_hi:[0,1]
	v_pk_mul_f32 v[58:59], v[92:93], v[198:199] op_sel_hi:[1,0]
	v_max_f32_e64 v0, |v62|, |v63|
	v_pk_fma_f32 v[58:59], v[78:79], v[58:59], v[88:89]
	v_add_u32_e32 v74, 0x80, v200
	v_pk_mul_f32 v[76:77], v[196:197], v[58:59] op_sel_hi:[0,1]
	v_max_f32_e64 v59, |v76|, |v77|
	v_max_f32_e64 v58, |v64|, |v65|
	v_max3_f32 v59, |v60|, |v61|, v59
	v_max3_f32 v0, v0, v58, v59
	v_mov_b32_e32 v58, v0
	s_nop 1
	v_permlane16_swap_b32_e32 v0, v58
	v_max_f32_e32 v0, v0, v58
	v_mov_b32_e32 v58, v0
	v_ashrrev_i32_e32 v75, 31, v74
	s_nop 0
	v_permlane32_swap_b32_e32 v0, v58
	v_lshlrev_b64 v[80:81], 8, v[74:75]
	v_max_f32_e32 v78, v0, v58
	v_lshl_add_u64 v[58:59], s[12:13], 0, v[80:81]
	s_and_saveexec_b64 s[0:1], s[4:5]
	s_cbranch_execz .LBB0_1388
	s_lshl_b32 s38, s14, 3
	s_ashr_i32 s39, s38, 31
	v_lshl_add_u64 v[80:81], s[38:39], 2, v[58:59]
	s_lshl_b32 s16, s52, 2
	v_lshl_add_u64 v[80:81], v[80:81], 0, s[16:17]
	v_mul_f32_e32 v0, 0x3c010204, v78
	global_store_dword v[80:81], v0, off
.LBB0_1388:
	s_or_b64 exec, exec, s[0:1]
	v_rcp_f32_e32 v0, v78
	v_cmp_lt_f32_e32 vcc, 0, v78
	v_lshlrev_b64 v[74:75], 11, v[74:75]
	v_cvt_f32_i32_e32 v55, v55
	v_mul_f32_e32 v0, 0x42fe0000, v0
	v_cndmask_b32_e32 v0, 0, v0, vcc
	v_pk_mul_f32 v[62:63], v[62:63], v[0:1] op_sel_hi:[1,0]
	v_pk_mul_f32 v[64:65], v[64:65], v[0:1] op_sel_hi:[1,0]
	v_pk_mul_f32 v[60:61], v[60:61], v[0:1] op_sel_hi:[1,0]
	v_pk_mul_f32 v[76:77], v[76:77], v[0:1] op_sel_hi:[1,0]
	v_add_f32_e32 v0, 0x4b400000, v62
	v_add_f32_e32 v62, 0x4b400000, v63
	v_add_f32_e32 v63, 0x4b400000, v64
	v_add_f32_e32 v64, 0x4b400000, v65
	v_perm_b32 v0, v62, v0, s59
	v_perm_b32 v62, v64, v63, s59
	v_lshl_or_b32 v62, v62, 16, v0
	v_add_f32_e32 v0, 0x4b400000, v60
	v_add_f32_e32 v60, 0x4b400000, v61
	v_add_f32_e32 v61, 0x4b400000, v76
	v_add_f32_e32 v63, 0x4b400000, v77
	v_perm_b32 v0, v60, v0, s59
	v_perm_b32 v60, v63, v61, s59
	v_cvt_f32_i32_e32 v54, v54
	v_lshl_or_b32 v63, v60, 16, v0
	v_lshl_add_u64 v[60:61], s[8:9], 0, v[74:75]
	v_cvt_f32_i32_e32 v57, v57
	v_cvt_f32_i32_e32 v56, v56
	v_mov_b32_e32 v199, v198
	v_lshl_add_u64 v[60:61], v[60:61], 0, v[176:177]
	v_cvt_f32_i32_e32 v51, v51
	v_cvt_f32_i32_e32 v50, v50
	global_store_dwordx2 v[60:61], v[62:63], off
	v_pk_mul_f32 v[62:63], v[94:95], v[198:199]
	v_cvt_f32_i32_e32 v53, v53
	v_cvt_f32_i32_e32 v52, v52
	v_pk_fma_f32 v[54:55], v[54:55], v[62:63], v[70:71]
	v_pk_mul_f32 v[62:63], v[96:97], v[198:199]
	v_mov_b32_e32 v197, v196
	v_pk_fma_f32 v[56:57], v[56:57], v[62:63], v[72:73]
	v_pk_mul_f32 v[62:63], v[82:83], v[198:199]
	v_pk_mul_f32 v[54:55], v[196:197], v[54:55]
	v_pk_fma_f32 v[50:51], v[50:51], v[62:63], v[66:67]
	v_pk_mul_f32 v[62:63], v[84:85], v[198:199]
	v_pk_mul_f32 v[56:57], v[196:197], v[56:57]
	v_pk_fma_f32 v[52:53], v[52:53], v[62:63], v[68:69]
	v_pk_mul_f32 v[50:51], v[196:197], v[50:51]
	v_pk_mul_f32 v[52:53], v[196:197], v[52:53]
	v_max_f32_e64 v0, |v54|, |v55|
	v_max_f32_e64 v63, |v52|, |v53|
	v_max_f32_e64 v62, |v56|, |v57|
	v_max3_f32 v63, |v50|, |v51|, v63
	v_max3_f32 v0, v0, v62, v63
	v_mov_b32_e32 v62, v0
	s_nop 1
	v_permlane16_swap_b32_e32 v0, v62
	v_max_f32_e32 v0, v0, v62
	v_mov_b32_e32 v62, v0
	s_nop 1
	v_permlane32_swap_b32_e32 v0, v62
	v_max_f32_e32 v62, v0, v62
	s_and_saveexec_b64 s[0:1], s[4:5]
	s_cbranch_execz .LBB0_1390
	s_lshl_b32 s38, s14, 3
	s_ashr_i32 s39, s38, 31
	v_lshl_add_u64 v[58:59], s[38:39], 2, v[58:59]
	s_lshl_b32 s16, s52, 2
	v_lshl_add_u64 v[58:59], v[58:59], 0, s[16:17]
	v_mul_f32_e32 v0, 0x3c010204, v62
	global_store_dword v[58:59], v0, off offset:16
.LBB0_1390:
	s_or_b64 exec, exec, s[0:1]
	v_rcp_f32_e32 v0, v62
	v_cmp_lt_f32_e32 vcc, 0, v62
	v_cvt_f32_i32_e32 v47, v47
	v_cvt_f32_i32_e32 v46, v46
	v_mul_f32_e32 v0, 0x42fe0000, v0
	v_cndmask_b32_e32 v0, 0, v0, vcc
	v_pk_mul_f32 v[54:55], v[54:55], v[0:1] op_sel_hi:[1,0]
	v_pk_mul_f32 v[56:57], v[56:57], v[0:1] op_sel_hi:[1,0]
	v_pk_mul_f32 v[50:51], v[50:51], v[0:1] op_sel_hi:[1,0]
	v_pk_mul_f32 v[52:53], v[52:53], v[0:1] op_sel_hi:[1,0]
	v_add_f32_e32 v0, 0x4b400000, v54
	v_add_f32_e32 v54, 0x4b400000, v55
	v_add_f32_e32 v55, 0x4b400000, v56
	v_add_f32_e32 v56, 0x4b400000, v57
	v_perm_b32 v0, v54, v0, s59
	v_perm_b32 v54, v56, v55, s59
	v_lshl_or_b32 v54, v54, 16, v0
	v_add_f32_e32 v0, 0x4b400000, v50
	v_add_f32_e32 v50, 0x4b400000, v51
	v_add_f32_e32 v51, 0x4b400000, v52
	v_add_f32_e32 v52, 0x4b400000, v53
	v_cvt_f32_i32_e32 v49, v49
	v_cvt_f32_i32_e32 v48, v48
	v_perm_b32 v0, v50, v0, s59
	v_perm_b32 v50, v52, v51, s59
	v_cvt_f32_i32_e32 v43, v43
	v_cvt_f32_i32_e32 v42, v42
	v_lshl_or_b32 v55, v50, 16, v0
	v_pk_mul_f32 v[50:51], v[102:103], v[192:193] op_sel_hi:[1,0]
	v_cvt_f32_i32_e32 v53, v45
	v_pk_fma_f32 v[46:47], v[46:47], v[50:51], v[98:99]
	v_pk_mul_f32 v[50:51], v[104:105], v[192:193] op_sel_hi:[1,0]
	v_cvt_f32_i32_e32 v52, v44
	v_pk_fma_f32 v[48:49], v[48:49], v[50:51], v[100:101]
	v_pk_mul_f32 v[50:51], v[90:91], v[192:193] op_sel_hi:[1,0]
	v_pk_mul_f32 v[46:47], v[190:191], v[46:47] op_sel_hi:[0,1]
	v_pk_fma_f32 v[42:43], v[42:43], v[50:51], v[86:87]
	v_pk_mul_f32 v[48:49], v[190:191], v[48:49] op_sel_hi:[0,1]
	v_pk_mul_f32 v[44:45], v[190:191], v[42:43] op_sel_hi:[0,1]
	v_pk_mul_f32 v[42:43], v[92:93], v[192:193] op_sel_hi:[1,0]
	v_max_f32_e64 v0, |v46|, |v47|
	v_pk_fma_f32 v[42:43], v[52:53], v[42:43], v[88:89]
	global_store_dwordx2 v[60:61], v[54:55], off offset:128
	v_pk_mul_f32 v[50:51], v[190:191], v[42:43] op_sel_hi:[0,1]
	v_max_f32_e64 v43, |v50|, |v51|
	v_max_f32_e64 v42, |v48|, |v49|
	v_max3_f32 v43, |v44|, |v45|, v43
	v_max3_f32 v0, v0, v42, v43
	v_mov_b32_e32 v42, v0
	s_nop 1
	v_permlane16_swap_b32_e32 v0, v42
	v_max_f32_e32 v0, v0, v42
	v_mov_b32_e32 v42, v0
	s_nop 1
	v_permlane32_swap_b32_e32 v0, v42
	v_lshlrev_b64 v[54:55], 8, v[194:195]
	v_max_f32_e32 v52, v0, v42
	v_lshl_add_u64 v[42:43], s[12:13], 0, v[54:55]
	s_and_saveexec_b64 s[0:1], s[4:5]
	s_cbranch_execz .LBB0_1392
	s_lshl_b32 s38, s14, 3
	s_ashr_i32 s39, s38, 31
	v_lshl_add_u64 v[54:55], s[38:39], 2, v[42:43]
	s_lshl_b32 s16, s52, 2
	v_lshl_add_u64 v[54:55], v[54:55], 0, s[16:17]
	v_mul_f32_e32 v0, 0x3c010204, v52
	global_store_dword v[54:55], v0, off
.LBB0_1392:
	s_or_b64 exec, exec, s[0:1]
	v_rcp_f32_e32 v0, v52
	v_cmp_lt_f32_e32 vcc, 0, v52
	v_lshlrev_b64 v[54:55], 11, v[194:195]
	v_cvt_f32_i32_e32 v39, v39
	v_mul_f32_e32 v0, 0x42fe0000, v0
	v_cndmask_b32_e32 v0, 0, v0, vcc
	v_pk_mul_f32 v[46:47], v[46:47], v[0:1] op_sel_hi:[1,0]
	v_pk_mul_f32 v[48:49], v[48:49], v[0:1] op_sel_hi:[1,0]
	v_pk_mul_f32 v[44:45], v[44:45], v[0:1] op_sel_hi:[1,0]
	v_pk_mul_f32 v[50:51], v[50:51], v[0:1] op_sel_hi:[1,0]
	v_add_f32_e32 v0, 0x4b400000, v46
	v_add_f32_e32 v46, 0x4b400000, v47
	v_add_f32_e32 v47, 0x4b400000, v48
	v_add_f32_e32 v48, 0x4b400000, v49
	v_perm_b32 v0, v46, v0, s59
	v_perm_b32 v46, v48, v47, s59
	v_lshl_or_b32 v46, v46, 16, v0
	v_add_f32_e32 v0, 0x4b400000, v44
	v_add_f32_e32 v44, 0x4b400000, v45
	v_add_f32_e32 v45, 0x4b400000, v50
	v_add_f32_e32 v47, 0x4b400000, v51
	v_perm_b32 v0, v44, v0, s59
	v_perm_b32 v44, v47, v45, s59
	v_cvt_f32_i32_e32 v38, v38
	v_lshl_or_b32 v47, v44, 16, v0
	v_lshl_add_u64 v[44:45], s[8:9], 0, v[54:55]
	v_cvt_f32_i32_e32 v41, v41
	v_cvt_f32_i32_e32 v40, v40
	v_mov_b32_e32 v193, v192
	v_lshl_add_u64 v[44:45], v[44:45], 0, v[176:177]
	v_cvt_f32_i32_e32 v35, v35
	v_cvt_f32_i32_e32 v34, v34
	global_store_dwordx2 v[44:45], v[46:47], off
	v_pk_mul_f32 v[46:47], v[94:95], v[192:193]
	v_cvt_f32_i32_e32 v37, v37
	v_cvt_f32_i32_e32 v36, v36
	v_pk_fma_f32 v[38:39], v[38:39], v[46:47], v[70:71]
	v_pk_mul_f32 v[46:47], v[96:97], v[192:193]
	v_mov_b32_e32 v191, v190
	v_pk_fma_f32 v[40:41], v[40:41], v[46:47], v[72:73]
	v_pk_mul_f32 v[46:47], v[82:83], v[192:193]
	v_pk_mul_f32 v[38:39], v[190:191], v[38:39]
	v_pk_fma_f32 v[34:35], v[34:35], v[46:47], v[66:67]
	v_pk_mul_f32 v[46:47], v[84:85], v[192:193]
	v_pk_mul_f32 v[40:41], v[190:191], v[40:41]
	v_pk_fma_f32 v[36:37], v[36:37], v[46:47], v[68:69]
	v_pk_mul_f32 v[34:35], v[190:191], v[34:35]
	v_pk_mul_f32 v[36:37], v[190:191], v[36:37]
	v_max_f32_e64 v0, |v38|, |v39|
	v_max_f32_e64 v47, |v36|, |v37|
	v_max_f32_e64 v46, |v40|, |v41|
	v_max3_f32 v47, |v34|, |v35|, v47
	v_max3_f32 v0, v0, v46, v47
	v_mov_b32_e32 v46, v0
	s_nop 1
	v_permlane16_swap_b32_e32 v0, v46
	v_max_f32_e32 v0, v0, v46
	v_mov_b32_e32 v46, v0
	s_nop 1
	v_permlane32_swap_b32_e32 v0, v46
	v_max_f32_e32 v46, v0, v46
	s_and_saveexec_b64 s[0:1], s[4:5]
	s_cbranch_execz .LBB0_1394
	s_lshl_b32 s38, s14, 3
	s_ashr_i32 s39, s38, 31
	v_lshl_add_u64 v[42:43], s[38:39], 2, v[42:43]
	s_lshl_b32 s16, s52, 2
	v_lshl_add_u64 v[42:43], v[42:43], 0, s[16:17]
	v_mul_f32_e32 v0, 0x3c010204, v46
	global_store_dword v[42:43], v0, off offset:16
.LBB0_1394:
	s_or_b64 exec, exec, s[0:1]
	v_rcp_f32_e32 v0, v46
	v_cmp_lt_f32_e32 vcc, 0, v46
	v_cvt_f32_i32_e32 v31, v31
	v_cvt_f32_i32_e32 v30, v30
	v_mul_f32_e32 v0, 0x42fe0000, v0
	v_cndmask_b32_e32 v0, 0, v0, vcc
	v_pk_mul_f32 v[38:39], v[38:39], v[0:1] op_sel_hi:[1,0]
	v_pk_mul_f32 v[40:41], v[40:41], v[0:1] op_sel_hi:[1,0]
	v_pk_mul_f32 v[34:35], v[34:35], v[0:1] op_sel_hi:[1,0]
	v_pk_mul_f32 v[36:37], v[36:37], v[0:1] op_sel_hi:[1,0]
	v_add_f32_e32 v0, 0x4b400000, v38
	v_add_f32_e32 v38, 0x4b400000, v39
	v_add_f32_e32 v39, 0x4b400000, v40
	v_add_f32_e32 v40, 0x4b400000, v41
	v_perm_b32 v0, v38, v0, s59
	v_perm_b32 v38, v40, v39, s59
	v_lshl_or_b32 v38, v38, 16, v0
	v_add_f32_e32 v0, 0x4b400000, v34
	v_add_f32_e32 v34, 0x4b400000, v35
	v_add_f32_e32 v35, 0x4b400000, v36
	v_add_f32_e32 v36, 0x4b400000, v37
	v_cvt_f32_i32_e32 v33, v33
	v_cvt_f32_i32_e32 v32, v32
	v_perm_b32 v0, v34, v0, s59
	v_perm_b32 v34, v36, v35, s59
	v_cvt_f32_i32_e32 v27, v27
	v_cvt_f32_i32_e32 v26, v26
	v_lshl_or_b32 v39, v34, 16, v0
	v_pk_mul_f32 v[34:35], v[102:103], v[186:187] op_sel_hi:[1,0]
	v_cvt_f32_i32_e32 v37, v29
	v_pk_fma_f32 v[30:31], v[30:31], v[34:35], v[98:99]
	v_pk_mul_f32 v[34:35], v[104:105], v[186:187] op_sel_hi:[1,0]
	v_cvt_f32_i32_e32 v36, v28
	v_pk_fma_f32 v[32:33], v[32:33], v[34:35], v[100:101]
	v_pk_mul_f32 v[34:35], v[90:91], v[186:187] op_sel_hi:[1,0]
	v_pk_mul_f32 v[30:31], v[184:185], v[30:31] op_sel_hi:[0,1]
	v_pk_fma_f32 v[26:27], v[26:27], v[34:35], v[86:87]
	v_pk_mul_f32 v[32:33], v[184:185], v[32:33] op_sel_hi:[0,1]
	v_pk_mul_f32 v[28:29], v[184:185], v[26:27] op_sel_hi:[0,1]
	v_pk_mul_f32 v[26:27], v[92:93], v[186:187] op_sel_hi:[1,0]
	v_max_f32_e64 v0, |v30|, |v31|
	v_pk_fma_f32 v[26:27], v[36:37], v[26:27], v[88:89]
	global_store_dwordx2 v[44:45], v[38:39], off offset:128
	v_pk_mul_f32 v[34:35], v[184:185], v[26:27] op_sel_hi:[0,1]
	v_max_f32_e64 v27, |v34|, |v35|
	v_max_f32_e64 v26, |v32|, |v33|
	v_max3_f32 v27, |v28|, |v29|, v27
	v_max3_f32 v0, v0, v26, v27
	v_mov_b32_e32 v26, v0
	s_nop 1
	v_permlane16_swap_b32_e32 v0, v26
	v_max_f32_e32 v0, v0, v26
	v_mov_b32_e32 v26, v0
	s_nop 1
	v_permlane32_swap_b32_e32 v0, v26
	v_lshlrev_b64 v[38:39], 8, v[188:189]
	v_max_f32_e32 v36, v0, v26
	v_lshl_add_u64 v[26:27], s[12:13], 0, v[38:39]
	s_and_saveexec_b64 s[0:1], s[4:5]
	s_cbranch_execz .LBB0_1396
	s_lshl_b32 s38, s14, 3
	s_ashr_i32 s39, s38, 31
	v_lshl_add_u64 v[38:39], s[38:39], 2, v[26:27]
	s_lshl_b32 s16, s52, 2
	v_lshl_add_u64 v[38:39], v[38:39], 0, s[16:17]
	v_mul_f32_e32 v0, 0x3c010204, v36
	global_store_dword v[38:39], v0, off
.LBB0_1396:
	s_or_b64 exec, exec, s[0:1]
	v_rcp_f32_e32 v0, v36
	v_cmp_lt_f32_e32 vcc, 0, v36
	v_lshlrev_b64 v[38:39], 11, v[188:189]
	v_cvt_f32_i32_e32 v23, v23
	v_mul_f32_e32 v0, 0x42fe0000, v0
	v_cndmask_b32_e32 v0, 0, v0, vcc
	v_pk_mul_f32 v[30:31], v[30:31], v[0:1] op_sel_hi:[1,0]
	v_pk_mul_f32 v[32:33], v[32:33], v[0:1] op_sel_hi:[1,0]
	v_pk_mul_f32 v[28:29], v[28:29], v[0:1] op_sel_hi:[1,0]
	v_pk_mul_f32 v[34:35], v[34:35], v[0:1] op_sel_hi:[1,0]
	v_add_f32_e32 v0, 0x4b400000, v30
	v_add_f32_e32 v30, 0x4b400000, v31
	v_add_f32_e32 v31, 0x4b400000, v32
	v_add_f32_e32 v32, 0x4b400000, v33
	v_perm_b32 v0, v30, v0, s59
	v_perm_b32 v30, v32, v31, s59
	v_lshl_or_b32 v30, v30, 16, v0
	v_add_f32_e32 v0, 0x4b400000, v28
	v_add_f32_e32 v28, 0x4b400000, v29
	v_add_f32_e32 v29, 0x4b400000, v34
	v_add_f32_e32 v31, 0x4b400000, v35
	v_perm_b32 v0, v28, v0, s59
	v_perm_b32 v28, v31, v29, s59
	v_cvt_f32_i32_e32 v22, v22
	v_lshl_or_b32 v31, v28, 16, v0
	v_lshl_add_u64 v[28:29], s[8:9], 0, v[38:39]
	v_cvt_f32_i32_e32 v25, v25
	v_cvt_f32_i32_e32 v24, v24
	v_mov_b32_e32 v187, v186
	v_lshl_add_u64 v[28:29], v[28:29], 0, v[176:177]
	v_cvt_f32_i32_e32 v19, v19
	v_cvt_f32_i32_e32 v18, v18
	global_store_dwordx2 v[28:29], v[30:31], off
	v_pk_mul_f32 v[30:31], v[94:95], v[186:187]
	v_cvt_f32_i32_e32 v21, v21
	v_cvt_f32_i32_e32 v20, v20
	v_pk_fma_f32 v[22:23], v[22:23], v[30:31], v[70:71]
	v_pk_mul_f32 v[30:31], v[96:97], v[186:187]
	v_mov_b32_e32 v185, v184
	v_pk_fma_f32 v[24:25], v[24:25], v[30:31], v[72:73]
	v_pk_mul_f32 v[30:31], v[82:83], v[186:187]
	v_pk_mul_f32 v[22:23], v[184:185], v[22:23]
	v_pk_fma_f32 v[18:19], v[18:19], v[30:31], v[66:67]
	v_pk_mul_f32 v[30:31], v[84:85], v[186:187]
	v_pk_mul_f32 v[24:25], v[184:185], v[24:25]
	v_pk_fma_f32 v[20:21], v[20:21], v[30:31], v[68:69]
	v_pk_mul_f32 v[18:19], v[184:185], v[18:19]
	v_pk_mul_f32 v[20:21], v[184:185], v[20:21]
	v_max_f32_e64 v0, |v22|, |v23|
	v_max_f32_e64 v31, |v20|, |v21|
	v_max_f32_e64 v30, |v24|, |v25|
	v_max3_f32 v31, |v18|, |v19|, v31
	v_max3_f32 v0, v0, v30, v31
	v_mov_b32_e32 v30, v0
	s_nop 1
	v_permlane16_swap_b32_e32 v0, v30
	v_max_f32_e32 v0, v0, v30
	v_mov_b32_e32 v30, v0
	s_nop 1
	v_permlane32_swap_b32_e32 v0, v30
	v_max_f32_e32 v30, v0, v30
	s_and_saveexec_b64 s[0:1], s[4:5]
	s_cbranch_execz .LBB0_1398
	s_lshl_b32 s38, s14, 3
	s_ashr_i32 s39, s38, 31
	v_lshl_add_u64 v[26:27], s[38:39], 2, v[26:27]
	s_lshl_b32 s16, s52, 2
	v_lshl_add_u64 v[26:27], v[26:27], 0, s[16:17]
	v_mul_f32_e32 v0, 0x3c010204, v30
	global_store_dword v[26:27], v0, off offset:16
.LBB0_1398:
	s_or_b64 exec, exec, s[0:1]
	v_rcp_f32_e32 v0, v30
	v_cmp_lt_f32_e32 vcc, 0, v30
	v_cvt_f32_i32_e32 v15, v15
	v_cvt_f32_i32_e32 v14, v14
	v_mul_f32_e32 v0, 0x42fe0000, v0
	v_cndmask_b32_e32 v0, 0, v0, vcc
	v_pk_mul_f32 v[22:23], v[22:23], v[0:1] op_sel_hi:[1,0]
	v_pk_mul_f32 v[24:25], v[24:25], v[0:1] op_sel_hi:[1,0]
	v_pk_mul_f32 v[18:19], v[18:19], v[0:1] op_sel_hi:[1,0]
	v_pk_mul_f32 v[20:21], v[20:21], v[0:1] op_sel_hi:[1,0]
	v_add_f32_e32 v0, 0x4b400000, v22
	v_add_f32_e32 v22, 0x4b400000, v23
	v_add_f32_e32 v23, 0x4b400000, v24
	v_add_f32_e32 v24, 0x4b400000, v25
	v_perm_b32 v0, v22, v0, s59
	v_perm_b32 v22, v24, v23, s59
	v_lshl_or_b32 v22, v22, 16, v0
	v_add_f32_e32 v0, 0x4b400000, v18
	v_add_f32_e32 v18, 0x4b400000, v19
	v_add_f32_e32 v19, 0x4b400000, v20
	v_add_f32_e32 v20, 0x4b400000, v21
	v_cvt_f32_i32_e32 v17, v17
	v_cvt_f32_i32_e32 v16, v16
	v_perm_b32 v0, v18, v0, s59
	v_perm_b32 v18, v20, v19, s59
	v_cvt_f32_i32_e32 v11, v11
	v_cvt_f32_i32_e32 v10, v10
	v_lshl_or_b32 v23, v18, 16, v0
	v_pk_mul_f32 v[18:19], v[102:103], v[180:181] op_sel_hi:[1,0]
	v_cvt_f32_i32_e32 v21, v13
	v_pk_fma_f32 v[14:15], v[14:15], v[18:19], v[98:99]
	v_pk_mul_f32 v[18:19], v[104:105], v[180:181] op_sel_hi:[1,0]
	v_cvt_f32_i32_e32 v20, v12
	v_pk_fma_f32 v[16:17], v[16:17], v[18:19], v[100:101]
	v_pk_mul_f32 v[18:19], v[90:91], v[180:181] op_sel_hi:[1,0]
	v_pk_mul_f32 v[14:15], v[178:179], v[14:15] op_sel_hi:[0,1]
	v_pk_fma_f32 v[10:11], v[10:11], v[18:19], v[86:87]
	v_pk_mul_f32 v[16:17], v[178:179], v[16:17] op_sel_hi:[0,1]
	v_pk_mul_f32 v[12:13], v[178:179], v[10:11] op_sel_hi:[0,1]
	v_pk_mul_f32 v[10:11], v[92:93], v[180:181] op_sel_hi:[1,0]
	v_max_f32_e64 v0, |v14|, |v15|
	v_pk_fma_f32 v[10:11], v[20:21], v[10:11], v[88:89]
	global_store_dwordx2 v[28:29], v[22:23], off offset:128
	v_pk_mul_f32 v[18:19], v[178:179], v[10:11] op_sel_hi:[0,1]
	v_max_f32_e64 v11, |v18|, |v19|
	v_max_f32_e64 v10, |v16|, |v17|
	v_max3_f32 v11, |v12|, |v13|, v11
	v_max3_f32 v0, v0, v10, v11
	v_mov_b32_e32 v10, v0
	s_nop 1
	v_permlane16_swap_b32_e32 v0, v10
	v_max_f32_e32 v0, v0, v10
	v_mov_b32_e32 v10, v0
	s_nop 1
	v_permlane32_swap_b32_e32 v0, v10
	v_lshlrev_b64 v[22:23], 8, v[182:183]
	v_max_f32_e32 v20, v0, v10
	v_lshl_add_u64 v[10:11], s[12:13], 0, v[22:23]
	s_and_saveexec_b64 s[0:1], s[4:5]
	s_cbranch_execz .LBB0_1400
	s_lshl_b32 s38, s14, 3
	s_ashr_i32 s39, s38, 31
	v_lshl_add_u64 v[22:23], s[38:39], 2, v[10:11]
	s_lshl_b32 s16, s52, 2
	v_lshl_add_u64 v[22:23], v[22:23], 0, s[16:17]
	v_mul_f32_e32 v0, 0x3c010204, v20
	global_store_dword v[22:23], v0, off
.LBB0_1400:
	s_or_b64 exec, exec, s[0:1]
	v_rcp_f32_e32 v0, v20
	v_cmp_lt_f32_e32 vcc, 0, v20
	v_lshlrev_b64 v[22:23], 11, v[182:183]
	v_cvt_f32_i32_e32 v7, v7
	v_mul_f32_e32 v0, 0x42fe0000, v0
	v_cndmask_b32_e32 v0, 0, v0, vcc
	v_pk_mul_f32 v[14:15], v[14:15], v[0:1] op_sel_hi:[1,0]
	v_pk_mul_f32 v[16:17], v[16:17], v[0:1] op_sel_hi:[1,0]
	v_pk_mul_f32 v[12:13], v[12:13], v[0:1] op_sel_hi:[1,0]
	v_pk_mul_f32 v[18:19], v[18:19], v[0:1] op_sel_hi:[1,0]
	v_add_f32_e32 v0, 0x4b400000, v14
	v_add_f32_e32 v14, 0x4b400000, v15
	v_add_f32_e32 v15, 0x4b400000, v16
	v_add_f32_e32 v16, 0x4b400000, v17
	v_perm_b32 v0, v14, v0, s59
	v_perm_b32 v14, v16, v15, s59
	v_lshl_or_b32 v14, v14, 16, v0
	v_add_f32_e32 v0, 0x4b400000, v12
	v_add_f32_e32 v12, 0x4b400000, v13
	v_add_f32_e32 v13, 0x4b400000, v18
	v_add_f32_e32 v15, 0x4b400000, v19
	v_perm_b32 v0, v12, v0, s59
	v_perm_b32 v12, v15, v13, s59
	v_cvt_f32_i32_e32 v6, v6
	v_lshl_or_b32 v15, v12, 16, v0
	v_lshl_add_u64 v[12:13], s[8:9], 0, v[22:23]
	v_cvt_f32_i32_e32 v9, v9
	v_cvt_f32_i32_e32 v8, v8
	v_mov_b32_e32 v181, v180
	v_lshl_add_u64 v[12:13], v[12:13], 0, v[176:177]
	v_cvt_f32_i32_e32 v3, v3
	v_cvt_f32_i32_e32 v2, v2
	global_store_dwordx2 v[12:13], v[14:15], off
	v_pk_mul_f32 v[14:15], v[94:95], v[180:181]
	v_cvt_f32_i32_e32 v5, v5
	v_cvt_f32_i32_e32 v4, v4
	v_pk_fma_f32 v[6:7], v[6:7], v[14:15], v[70:71]
	v_pk_mul_f32 v[14:15], v[96:97], v[180:181]
	v_mov_b32_e32 v179, v178
	v_pk_fma_f32 v[8:9], v[8:9], v[14:15], v[72:73]
	v_pk_mul_f32 v[14:15], v[82:83], v[180:181]
	v_pk_mul_f32 v[6:7], v[178:179], v[6:7]
	v_pk_fma_f32 v[2:3], v[2:3], v[14:15], v[66:67]
	v_pk_mul_f32 v[14:15], v[84:85], v[180:181]
	v_pk_mul_f32 v[8:9], v[178:179], v[8:9]
	v_pk_fma_f32 v[4:5], v[4:5], v[14:15], v[68:69]
	v_pk_mul_f32 v[2:3], v[178:179], v[2:3]
	v_pk_mul_f32 v[4:5], v[178:179], v[4:5]
	v_max_f32_e64 v0, |v6|, |v7|
	v_max_f32_e64 v15, |v4|, |v5|
	v_max_f32_e64 v14, |v8|, |v9|
	v_max3_f32 v15, |v2|, |v3|, v15
	v_max3_f32 v0, v0, v14, v15
	v_mov_b32_e32 v14, v0
	s_nop 1
	v_permlane16_swap_b32_e32 v0, v14
	v_max_f32_e32 v0, v0, v14
	v_mov_b32_e32 v14, v0
	s_nop 1
	v_permlane32_swap_b32_e32 v0, v14
	v_max_f32_e32 v14, v0, v14
	s_and_saveexec_b64 s[0:1], s[4:5]
	s_cbranch_execz .LBB0_1402
	s_lshl_b32 s38, s14, 3
	s_ashr_i32 s39, s38, 31
	v_lshl_add_u64 v[10:11], s[38:39], 2, v[10:11]
	s_lshl_b32 s16, s52, 2
	v_lshl_add_u64 v[10:11], v[10:11], 0, s[16:17]
	v_mul_f32_e32 v0, 0x3c010204, v14
	global_store_dword v[10:11], v0, off offset:16

.LBB0_1406:
	s_waitcnt vmcnt(0)
	s_barrier
	s_mov_b64 s[0:1], exec
	v_readlane_b32 s2, v252, 11
	v_readlane_b32 s3, v252, 12
	s_and_b64 s[2:3], s[0:1], s[2:3]
	s_mov_b64 exec, s[2:3]
	s_cbranch_execz .LBB0_1458
	s_add_i32 s2, 0, 0x26f20
	v_mov_b32_e32 v0, s2
	s_waitcnt vmcnt(0) expcnt(0) lgkmcnt(0)
	ds_read_b32 v3, v0
	s_add_i32 s2, 0, 0x26f24
	v_mov_b32_e32 v0, s2
	ds_read_b32 v1, v0
	s_waitcnt lgkmcnt(1)
	v_cmp_ne_u32_e32 vcc, 0, v3
	s_cbranch_vccnz .LBB0_1422
	v_readlane_b32 s2, v252, 4
	v_readlane_b32 s3, v252, 5
	s_load_dwordx2 s[6:7], s[2:3], 0x4
	v_readlane_b32 s40, v252, 2
	v_readlane_b32 s41, v252, 3
	s_add_u32 s2, s40, 0x4200
	s_addc_u32 s3, s41, 0
	s_add_u32 s4, s40, 0x4400
	s_addc_u32 s5, s41, 0
	v_readlane_b32 s10, v252, 6
	s_waitcnt lgkmcnt(0)
	s_mul_i32 s33, s6, s10
	s_add_u32 s6, s40, 0x4500
	s_mul_i32 s33, s33, s7
	s_addc_u32 s7, s41, 0
	v_readlane_b32 s11, v252, 7
	s_add_u32 s10, s40, 0x4600
	s_addc_u32 s11, s41, 0
	s_add_u32 s14, s40, 0x4700
	s_addc_u32 s15, s41, 0
	s_add_u32 s16, s40, 0x4800
	s_addc_u32 s17, s41, 0
	s_add_u32 s18, s40, 0x4900
	s_addc_u32 s19, s41, 0
	s_add_u32 s20, s40, 0x4a00
	s_addc_u32 s21, s41, 0
	s_add_u32 s22, s40, 0x4b00
	s_addc_u32 s23, s41, 0
	s_add_u32 s24, s40, 0x4c00
	s_addc_u32 s25, s41, 0
	s_add_u32 s26, s40, 0x4d00
	s_addc_u32 s27, s41, 0
	s_add_u32 s28, s40, 0x4e00
	s_addc_u32 s29, s41, 0
	s_add_u32 s30, s40, 0x4f00
	s_addc_u32 s31, s41, 0
	s_add_u32 s34, s40, 0x5000
	s_addc_u32 s35, s41, 0
	s_add_u32 s36, s40, 0x5100
	s_addc_u32 s37, s41, 0
	s_add_u32 s38, s40, 0x5200
	s_addc_u32 s39, s41, 0
	s_add_u32 s40, s40, 0x5300
	s_addc_u32 s41, s41, 0
	s_mov_b32 s48, 1
	v_mov_b32_e32 v17, 0
	s_branch .LBB0_1410
	s_nop 0
	s_nop 0
	s_nop 0
	s_nop 0
	s_nop 0
	s_nop 0
	s_nop 0
	s_nop 0
	s_nop 0
	s_nop 0
	s_nop 0
	s_nop 0
	s_nop 0
	s_nop 0
	s_nop 0
	s_nop 0
	s_nop 0
	s_nop 0
	s_nop 0
	s_nop 0
	s_nop 0
	s_nop 0
	s_nop 0
	s_nop 0
	s_nop 0
	s_nop 0
	s_nop 0
	s_nop 0
	s_nop 0
	s_nop 0
	s_nop 0
	s_nop 0
	s_nop 0
	s_nop 0
	s_nop 0
	s_nop 0
	s_nop 0
	s_nop 0
	s_nop 0
	s_nop 0
	s_nop 0
	s_nop 0
	s_nop 0
	s_nop 0
	s_nop 0
	s_nop 0
	s_nop 0
	s_nop 0
	s_nop 0
	s_nop 0
	s_nop 0
	s_nop 0
	s_nop 0
	s_nop 0
	s_nop 0
	s_nop 0
	s_nop 0
	s_nop 0
	s_nop 0
	s_nop 0
	s_nop 0
	s_nop 0
	s_nop 0
	s_nop 0
